# stack + GEMM K-loops: first iteration peeled with zero C operand on each accumulator's first MFMA, accumulator zeroing removed
# speedup vs baseline: 1.0459x; 1.0009x over previous
.LBB0_161:
	s_ashr_i32 s29, s28, 31
	s_lshl_b64 s[30:31], s[28:29], 20
	v_readlane_b32 s34, v254, 18
	v_readlane_b32 s35, v254, 19
	s_add_u32 s30, s34, s30
	s_addc_u32 s31, s35, s31
	s_and_b64 s[34:35], s[12:13], exec
	s_cselect_b32 s15, s31, s17
	s_cselect_b32 s29, s30, s16
	s_ashr_i32 s27, s26, 31
	s_lshl_b64 s[34:35], s[26:27], 20
	s_add_u32 s34, s33, s34
	s_addc_u32 s35, s42, s35
	s_and_b64 s[38:39], s[12:13], exec
	s_cselect_b32 s27, s35, s37
	s_cselect_b32 s40, s34, s36
	s_add_u32 s16, s16, 0x80080
	s_addc_u32 s17, s17, 0
	s_add_u32 s41, s36, 0x100
	s_addc_u32 s64, s37, 0
	s_mov_b32 s65, -2
	ds_read_b128 v[90:93], v197
	ds_read_b128 v[94:97], v197 offset:1024
	ds_read_b128 v[98:101], v197 offset:2048
	ds_read_b128 v[102:105], v197 offset:3072
	ds_read_b128 v[146:149], v198
	ds_read_b128 v[150:153], v198 offset:1024
	ds_read_b128 v[180:183], v198 offset:2048
	ds_read_b128 v[184:187], v198 offset:3072
	s_add_u32 s36, s16, 0xfff80080
	s_addc_u32 s37, s17, -1
	s_cmp_eq_u32 s65, 28
	s_cselect_b32 s39, s15, s37
	s_cselect_b32 s38, s29, s36
	s_cselect_b32 s37, s27, s64
	s_cselect_b32 s36, s40, s41
	v_lshl_add_u64 v[212:213], s[16:17], 0, v[172:173]
	s_add_i32 m0, s44, 0xc000
	ds_read_b128 v[188:191], v199
	ds_read_b128 v[192:195], v199 offset:1024
	ds_read_b128 v[200:203], v199 offset:2048
	ds_read_b128 v[204:207], v199 offset:3072
	ds_read_b128 v[208:211], v199 offset:4096
	ds_read_b128 v[216:219], v199 offset:5120
	ds_read_b128 v[220:223], v199 offset:6144
	ds_read_b128 v[224:227], v199 offset:7168
	global_load_lds_dwordx4 v[212:213], off
	v_lshl_add_u64 v[212:213], s[16:17], 0, v[174:175]
	s_add_i32 m0, s44, 0xe000
	s_nop 0
	global_load_lds_dwordx4 v[212:213], off
	s_waitcnt vmcnt(8)
	s_waitcnt lgkmcnt(0)
	s_setprio 1
	s_barrier
	v_mfma_f32_16x16x32_bf16 v[70:73], v[90:93], v[188:191], 0
	v_mfma_f32_16x16x32_bf16 v[66:69], v[98:101], v[188:191], 0
	v_mfma_f32_16x16x32_bf16 v[54:57], v[90:93], v[200:203], 0
	v_mfma_f32_16x16x32_bf16 v[50:53], v[98:101], v[200:203], 0
	v_mfma_f32_16x16x32_bf16 v[46:49], v[90:93], v[208:211], 0
	v_mfma_f32_16x16x32_bf16 v[42:45], v[98:101], v[208:211], 0
	v_mfma_f32_16x16x32_bf16 v[38:41], v[90:93], v[220:223], 0
	v_mfma_f32_16x16x32_bf16 v[34:37], v[98:101], v[220:223], 0
	v_mfma_f32_16x16x32_bf16 v[70:73], v[94:97], v[192:195], v[70:73]
	v_mfma_f32_16x16x32_bf16 v[66:69], v[102:105], v[192:195], v[66:69]
	v_mfma_f32_16x16x32_bf16 v[54:57], v[94:97], v[204:207], v[54:57]
	v_mfma_f32_16x16x32_bf16 v[50:53], v[102:105], v[204:207], v[50:53]
	v_mfma_f32_16x16x32_bf16 v[46:49], v[94:97], v[216:219], v[46:49]
	v_mfma_f32_16x16x32_bf16 v[42:45], v[102:105], v[216:219], v[42:45]
	v_mfma_f32_16x16x32_bf16 v[38:41], v[94:97], v[224:227], v[38:41]
	v_mfma_f32_16x16x32_bf16 v[34:37], v[102:105], v[224:227], v[34:37]
	s_setprio 0
	s_setprio 1
	v_mfma_f32_16x16x32_bf16 v[142:145], v[146:149], v[188:191], 0
	v_mfma_f32_16x16x32_bf16 v[138:141], v[180:183], v[188:191], 0
	v_mfma_f32_16x16x32_bf16 v[134:137], v[146:149], v[200:203], 0
	v_mfma_f32_16x16x32_bf16 v[130:133], v[180:183], v[200:203], 0
	v_mfma_f32_16x16x32_bf16 v[126:129], v[146:149], v[208:211], 0
	v_mfma_f32_16x16x32_bf16 v[122:125], v[180:183], v[208:211], 0
	v_mfma_f32_16x16x32_bf16 v[118:121], v[146:149], v[220:223], 0
	v_mfma_f32_16x16x32_bf16 v[114:117], v[180:183], v[220:223], 0
	v_mfma_f32_16x16x32_bf16 v[142:145], v[150:153], v[192:195], v[142:145]
	v_mfma_f32_16x16x32_bf16 v[138:141], v[184:187], v[192:195], v[138:141]
	v_mfma_f32_16x16x32_bf16 v[134:137], v[150:153], v[204:207], v[134:137]
	v_mfma_f32_16x16x32_bf16 v[130:133], v[184:187], v[204:207], v[130:133]
	v_mfma_f32_16x16x32_bf16 v[126:129], v[150:153], v[216:219], v[126:129]
	v_mfma_f32_16x16x32_bf16 v[122:125], v[184:187], v[216:219], v[122:125]
	v_mfma_f32_16x16x32_bf16 v[118:121], v[150:153], v[224:227], v[118:121]
	v_mfma_f32_16x16x32_bf16 v[114:117], v[184:187], v[224:227], v[114:117]
	s_barrier
	s_setprio 0
	s_add_i32 s66, s57, s43
	v_lshl_add_u64 v[212:213], s[36:37], 0, v[156:157]
	s_mov_b32 m0, s66
	ds_read_b128 v[188:191], v199 offset:16384
	ds_read_b128 v[192:195], v199 offset:17408
	ds_read_b128 v[200:203], v199 offset:18432
	ds_read_b128 v[204:207], v199 offset:19456
	ds_read_b128 v[208:211], v199 offset:20480
	ds_read_b128 v[216:219], v199 offset:21504
	ds_read_b128 v[220:223], v199 offset:22528
	ds_read_b128 v[224:227], v199 offset:23552
	global_load_lds_dwordx4 v[212:213], off
	s_add_i32 m0, s66, 0x2000
	s_add_u32 s66, s36, 0x80000
	v_lshl_add_u64 v[214:215], s[36:37], 0, v[160:161]
	s_addc_u32 s67, s37, 0
	s_add_i32 s68, s58, s43
	global_load_lds_dwordx4 v[214:215], off
	v_lshl_add_u64 v[228:229], s[66:67], 0, v[156:157]
	s_mov_b32 m0, s68
	v_lshl_add_u64 v[230:231], s[38:39], 0, v[158:159]
	global_load_lds_dwordx4 v[228:229], off
	v_lshl_add_u64 v[228:229], s[66:67], 0, v[160:161]
	s_add_i32 m0, s68, 0x2000
	s_nop 0
	global_load_lds_dwordx4 v[228:229], off
	v_lshl_add_u64 v[228:229], s[38:39], 0, v[154:155]
	s_mov_b32 m0, s44
	s_nop 0
	global_load_lds_dwordx4 v[228:229], off
	s_mov_b32 m0, s45
	s_nop 0
	global_load_lds_dwordx4 v[230:231], off
	s_waitcnt vmcnt(8)
	s_waitcnt lgkmcnt(0)
	s_setprio 1
	s_barrier
	v_mfma_f32_16x16x32_bf16 v[30:33], v[90:93], v[188:191], 0
	v_mfma_f32_16x16x32_bf16 v[26:29], v[98:101], v[188:191], 0
	v_mfma_f32_16x16x32_bf16 v[22:25], v[90:93], v[200:203], 0
	v_mfma_f32_16x16x32_bf16 v[18:21], v[98:101], v[200:203], 0
	v_mfma_f32_16x16x32_bf16 v[14:17], v[90:93], v[208:211], 0
	v_mfma_f32_16x16x32_bf16 v[10:13], v[98:101], v[208:211], 0
	v_mfma_f32_16x16x32_bf16 v[6:9], v[90:93], v[220:223], 0
	v_mfma_f32_16x16x32_bf16 v[2:5], v[98:101], v[220:223], 0
	v_mfma_f32_16x16x32_bf16 v[30:33], v[94:97], v[192:195], v[30:33]
	v_mfma_f32_16x16x32_bf16 v[26:29], v[102:105], v[192:195], v[26:29]
	v_mfma_f32_16x16x32_bf16 v[22:25], v[94:97], v[204:207], v[22:25]
	v_mfma_f32_16x16x32_bf16 v[18:21], v[102:105], v[204:207], v[18:21]
	v_mfma_f32_16x16x32_bf16 v[14:17], v[94:97], v[216:219], v[14:17]
	v_mfma_f32_16x16x32_bf16 v[10:13], v[102:105], v[216:219], v[10:13]
	v_mfma_f32_16x16x32_bf16 v[6:9], v[94:97], v[224:227], v[6:9]
	v_mfma_f32_16x16x32_bf16 v[2:5], v[102:105], v[224:227], v[2:5]
	s_setprio 0
	s_setprio 1
	v_mfma_f32_16x16x32_bf16 v[86:89], v[146:149], v[200:203], 0
	v_mfma_f32_16x16x32_bf16 v[82:85], v[180:183], v[200:203], 0
	v_mfma_f32_16x16x32_bf16 v[78:81], v[146:149], v[208:211], 0
	v_mfma_f32_16x16x32_bf16 v[74:77], v[180:183], v[208:211], 0
	v_mfma_f32_16x16x32_bf16 v[62:65], v[146:149], v[220:223], 0
	v_mfma_f32_16x16x32_bf16 v[58:61], v[180:183], v[220:223], 0
	v_mfma_f32_16x16x32_bf16 v[90:93], v[146:149], v[188:191], 0
	v_mfma_f32_16x16x32_bf16 v[94:97], v[180:183], v[188:191], 0
	v_mfma_f32_16x16x32_bf16 v[86:89], v[150:153], v[204:207], v[86:89]
	v_mfma_f32_16x16x32_bf16 v[82:85], v[184:187], v[204:207], v[82:85]
	v_mfma_f32_16x16x32_bf16 v[78:81], v[150:153], v[216:219], v[78:81]
	v_mfma_f32_16x16x32_bf16 v[74:77], v[184:187], v[216:219], v[74:77]
	v_mfma_f32_16x16x32_bf16 v[62:65], v[150:153], v[224:227], v[62:65]
	v_mfma_f32_16x16x32_bf16 v[58:61], v[184:187], v[224:227], v[58:61]
	v_mfma_f32_16x16x32_bf16 v[90:93], v[150:153], v[192:195], v[90:93]
	v_mfma_f32_16x16x32_bf16 v[94:97], v[184:187], v[192:195], v[94:97]
	s_barrier
	s_setprio 0
	s_add_i32 s66, 0, 0x18000
	s_add_i32 s67, 0, 0x1c000
	v_add_u32_e32 v110, s66, v165
	v_add_u32_e32 v162, s67, v165
	ds_read_b128 v[98:101], v110
	ds_read_b128 v[102:105], v110 offset:1024
	ds_read_b128 v[106:109], v110 offset:2048
	ds_read_b128 v[110:113], v110 offset:3072
	ds_read_b128 v[146:149], v162
	ds_read_b128 v[150:153], v162 offset:1024
	ds_read_b128 v[180:183], v162 offset:2048
	ds_read_b128 v[184:187], v162 offset:3072
	s_add_u32 s38, s38, 0x80000
	s_addc_u32 s39, s39, 0
	s_mov_b32 m0, s47
	v_lshl_add_u64 v[232:233], s[38:39], 0, v[154:155]
	ds_read_b128 v[188:191], v199 offset:32768
	ds_read_b128 v[192:195], v199 offset:33792
	ds_read_b128 v[200:203], v199 offset:34816
	ds_read_b128 v[204:207], v199 offset:35840
	ds_read_b128 v[208:211], v199 offset:36864
	ds_read_b128 v[216:219], v199 offset:37888
	ds_read_b128 v[220:223], v199 offset:38912
	ds_read_b128 v[224:227], v199 offset:39936
	global_load_lds_dwordx4 v[232:233], off
	v_lshl_add_u64 v[232:233], s[38:39], 0, v[158:159]
	s_mov_b32 m0, s48
	s_nop 0
	global_load_lds_dwordx4 v[232:233], off
	s_waitcnt vmcnt(8)
	s_waitcnt lgkmcnt(0)
	s_setprio 1
	s_barrier
	v_mfma_f32_16x16x32_bf16 v[70:73], v[98:101], v[188:191], v[70:73]
	v_mfma_f32_16x16x32_bf16 v[66:69], v[106:109], v[188:191], v[66:69]
	v_mfma_f32_16x16x32_bf16 v[54:57], v[98:101], v[200:203], v[54:57]
	v_mfma_f32_16x16x32_bf16 v[50:53], v[106:109], v[200:203], v[50:53]
	v_mfma_f32_16x16x32_bf16 v[46:49], v[98:101], v[208:211], v[46:49]
	v_mfma_f32_16x16x32_bf16 v[42:45], v[106:109], v[208:211], v[42:45]
	v_mfma_f32_16x16x32_bf16 v[38:41], v[98:101], v[220:223], v[38:41]
	v_mfma_f32_16x16x32_bf16 v[34:37], v[106:109], v[220:223], v[34:37]
	v_mfma_f32_16x16x32_bf16 v[70:73], v[102:105], v[192:195], v[70:73]
	v_mfma_f32_16x16x32_bf16 v[66:69], v[110:113], v[192:195], v[66:69]
	v_mfma_f32_16x16x32_bf16 v[54:57], v[102:105], v[204:207], v[54:57]
	v_mfma_f32_16x16x32_bf16 v[50:53], v[110:113], v[204:207], v[50:53]
	v_mfma_f32_16x16x32_bf16 v[46:49], v[102:105], v[216:219], v[46:49]
	v_mfma_f32_16x16x32_bf16 v[42:45], v[110:113], v[216:219], v[42:45]
	v_mfma_f32_16x16x32_bf16 v[38:41], v[102:105], v[224:227], v[38:41]
	v_mfma_f32_16x16x32_bf16 v[34:37], v[110:113], v[224:227], v[34:37]
	s_setprio 0
	s_setprio 1
	v_mfma_f32_16x16x32_bf16 v[142:145], v[146:149], v[188:191], v[142:145]
	v_mfma_f32_16x16x32_bf16 v[138:141], v[180:183], v[188:191], v[138:141]
	v_mfma_f32_16x16x32_bf16 v[134:137], v[146:149], v[200:203], v[134:137]
	v_mfma_f32_16x16x32_bf16 v[130:133], v[180:183], v[200:203], v[130:133]
	v_mfma_f32_16x16x32_bf16 v[126:129], v[146:149], v[208:211], v[126:129]
	v_mfma_f32_16x16x32_bf16 v[122:125], v[180:183], v[208:211], v[122:125]
	v_mfma_f32_16x16x32_bf16 v[118:121], v[146:149], v[220:223], v[118:121]
	v_mfma_f32_16x16x32_bf16 v[114:117], v[180:183], v[220:223], v[114:117]
	v_mfma_f32_16x16x32_bf16 v[142:145], v[150:153], v[192:195], v[142:145]
	v_mfma_f32_16x16x32_bf16 v[138:141], v[184:187], v[192:195], v[138:141]
	v_mfma_f32_16x16x32_bf16 v[134:137], v[150:153], v[204:207], v[134:137]
	v_mfma_f32_16x16x32_bf16 v[130:133], v[184:187], v[204:207], v[130:133]
	v_mfma_f32_16x16x32_bf16 v[126:129], v[150:153], v[216:219], v[126:129]
	v_mfma_f32_16x16x32_bf16 v[122:125], v[184:187], v[216:219], v[122:125]
	v_mfma_f32_16x16x32_bf16 v[118:121], v[150:153], v[224:227], v[118:121]
	v_mfma_f32_16x16x32_bf16 v[114:117], v[184:187], v[224:227], v[114:117]
	s_barrier
	s_setprio 0
	s_add_i32 s38, s66, s43
	v_lshl_add_u64 v[212:213], v[212:213], 0, s[18:19]
	s_mov_b32 m0, s38
	ds_read_b128 v[188:191], v199 offset:49152
	ds_read_b128 v[192:195], v199 offset:50176
	ds_read_b128 v[200:203], v199 offset:51200
	ds_read_b128 v[204:207], v199 offset:52224
	ds_read_b128 v[208:211], v199 offset:53248
	ds_read_b128 v[216:219], v199 offset:54272
	ds_read_b128 v[220:223], v199 offset:55296
	ds_read_b128 v[224:227], v199 offset:56320
	global_load_lds_dwordx4 v[212:213], off
	s_add_i32 m0, s38, 0x2000
	s_add_u32 s36, s36, 0x80080
	v_lshl_add_u64 v[212:213], v[214:215], 0, s[18:19]
	s_addc_u32 s37, s37, 0
	s_add_i32 s38, s67, s43
	global_load_lds_dwordx4 v[212:213], off
	v_lshl_add_u64 v[212:213], s[36:37], 0, v[156:157]
	s_mov_b32 m0, s38
	s_nop 0
	global_load_lds_dwordx4 v[212:213], off
	v_lshl_add_u64 v[212:213], s[36:37], 0, v[160:161]
	s_add_i32 m0, s38, 0x2000
	s_nop 0
	global_load_lds_dwordx4 v[212:213], off
	v_lshl_add_u64 v[212:213], v[228:229], 0, s[18:19]
	s_mov_b32 m0, s52
	s_nop 0
	global_load_lds_dwordx4 v[212:213], off
	v_lshl_add_u64 v[212:213], v[230:231], 0, s[18:19]
	s_mov_b32 m0, s53
	s_nop 0
	global_load_lds_dwordx4 v[212:213], off
	s_waitcnt vmcnt(8)
	s_waitcnt lgkmcnt(0)
	s_setprio 1
	s_barrier
	v_mfma_f32_16x16x32_bf16 v[30:33], v[98:101], v[188:191], v[30:33]
	v_mfma_f32_16x16x32_bf16 v[26:29], v[106:109], v[188:191], v[26:29]
	v_mfma_f32_16x16x32_bf16 v[22:25], v[98:101], v[200:203], v[22:25]
	v_mfma_f32_16x16x32_bf16 v[18:21], v[106:109], v[200:203], v[18:21]
	v_mfma_f32_16x16x32_bf16 v[14:17], v[98:101], v[208:211], v[14:17]
	v_mfma_f32_16x16x32_bf16 v[10:13], v[106:109], v[208:211], v[10:13]
	v_mfma_f32_16x16x32_bf16 v[6:9], v[98:101], v[220:223], v[6:9]
	v_mfma_f32_16x16x32_bf16 v[2:5], v[106:109], v[220:223], v[2:5]
	v_mfma_f32_16x16x32_bf16 v[30:33], v[102:105], v[192:195], v[30:33]
	v_mfma_f32_16x16x32_bf16 v[26:29], v[110:113], v[192:195], v[26:29]
	v_mfma_f32_16x16x32_bf16 v[22:25], v[102:105], v[204:207], v[22:25]
	v_mfma_f32_16x16x32_bf16 v[18:21], v[110:113], v[204:207], v[18:21]
	v_mfma_f32_16x16x32_bf16 v[14:17], v[102:105], v[216:219], v[14:17]
	v_mfma_f32_16x16x32_bf16 v[10:13], v[110:113], v[216:219], v[10:13]
	v_mfma_f32_16x16x32_bf16 v[6:9], v[102:105], v[224:227], v[6:9]
	v_mfma_f32_16x16x32_bf16 v[2:5], v[110:113], v[224:227], v[2:5]
	s_setprio 0
	s_setprio 1
	v_mfma_f32_16x16x32_bf16 v[90:93], v[146:149], v[188:191], v[90:93]
	v_mfma_f32_16x16x32_bf16 v[110:113], v[150:153], v[192:195], v[90:93]
	v_mfma_f32_16x16x32_bf16 v[90:93], v[180:183], v[188:191], v[94:97]
	v_mfma_f32_16x16x32_bf16 v[86:89], v[146:149], v[200:203], v[86:89]
	v_mfma_f32_16x16x32_bf16 v[82:85], v[180:183], v[200:203], v[82:85]
	v_mfma_f32_16x16x32_bf16 v[78:81], v[146:149], v[208:211], v[78:81]
	v_mfma_f32_16x16x32_bf16 v[74:77], v[180:183], v[208:211], v[74:77]
	v_mfma_f32_16x16x32_bf16 v[62:65], v[146:149], v[220:223], v[62:65]
	v_mfma_f32_16x16x32_bf16 v[58:61], v[180:183], v[220:223], v[58:61]
	v_mfma_f32_16x16x32_bf16 v[106:109], v[184:187], v[192:195], v[90:93]
	v_mfma_f32_16x16x32_bf16 v[86:89], v[150:153], v[204:207], v[86:89]
	v_mfma_f32_16x16x32_bf16 v[82:85], v[184:187], v[204:207], v[82:85]
	v_mfma_f32_16x16x32_bf16 v[78:81], v[150:153], v[216:219], v[78:81]
	v_mfma_f32_16x16x32_bf16 v[74:77], v[184:187], v[216:219], v[74:77]
	v_mfma_f32_16x16x32_bf16 v[62:65], v[150:153], v[224:227], v[62:65]
	v_mfma_f32_16x16x32_bf16 v[58:61], v[184:187], v[224:227], v[58:61]
	s_barrier
	s_setprio 0
	s_add_i32 s65, s65, 2
	s_add_u32 s16, s16, 0x100
	s_addc_u32 s17, s17, 0
	s_add_u32 s41, s41, 0x100
	s_addc_u32 s64, s64, 0
	s_cmp_gt_u32 s65, 29

.LBB0_427:
	s_ashr_i32 s25, s24, 31
	s_lshl_b64 s[8:9], s[24:25], 20
	s_add_u32 s10, s86, s8
	s_addc_u32 s11, s87, s9
	s_and_b64 s[8:9], s[34:35], exec
	s_cselect_b32 s25, s11, s1
	s_cselect_b32 s55, s10, s0
	s_ashr_i32 s27, s26, 31
	s_lshl_b64 s[8:9], s[26:27], 20
	s_add_u32 s8, s86, s8
	s_addc_u32 s9, s87, s9
	s_and_b64 s[34:35], s[34:35], exec
	s_cselect_b32 s27, s9, s31
	s_cselect_b32 s56, s8, s30
	s_add_u32 s0, s0, 0x80080
	s_addc_u32 s1, s1, 0
	s_add_u32 s57, s30, 0x100
	s_addc_u32 s58, s31, 0
	s_mov_b32 s59, -2
	ds_read_b128 v[150:153], v146
	ds_read_b128 v[154:157], v146 offset:1024
	ds_read_b128 v[158:161], v146 offset:2048
	ds_read_b128 v[162:165], v146 offset:3072
	ds_read_b128 v[166:169], v147
	ds_read_b128 v[170:173], v147 offset:1024
	ds_read_b128 v[174:177], v147 offset:2048
	ds_read_b128 v[178:181], v147 offset:3072
	s_add_u32 s30, s0, 0xfff80080
	s_addc_u32 s31, s1, -1
	s_cmp_eq_u32 s59, 28
	s_cselect_b32 s35, s25, s31
	s_cselect_b32 s34, s55, s30
	s_cselect_b32 s31, s27, s58
	s_cselect_b32 s30, s56, s57
	v_lshl_add_u64 v[142:143], s[0:1], 0, v[138:139]
	s_add_i32 m0, s39, 0xc000
	ds_read_b128 v[182:185], v148
	ds_read_b128 v[186:189], v148 offset:1024
	ds_read_b128 v[190:193], v148 offset:2048
	ds_read_b128 v[194:197], v148 offset:3072
	ds_read_b128 v[198:201], v148 offset:4096
	ds_read_b128 v[202:205], v148 offset:5120
	ds_read_b128 v[206:209], v148 offset:6144
	ds_read_b128 v[210:213], v148 offset:7168
	global_load_lds_dwordx4 v[142:143], off
	v_lshl_add_u64 v[142:143], s[0:1], 0, v[140:141]
	s_add_i32 m0, s39, 0xe000
	s_nop 0
	global_load_lds_dwordx4 v[142:143], off
	s_waitcnt vmcnt(8)
	s_waitcnt lgkmcnt(0)
	s_setprio 1
	s_barrier
	v_mfma_f32_16x16x32_bf16 v[94:97], v[150:153], v[182:185], 0
	v_mfma_f32_16x16x32_bf16 v[86:89], v[158:161], v[182:185], 0
	v_mfma_f32_16x16x32_bf16 v[66:69], v[150:153], v[190:193], 0
	v_mfma_f32_16x16x32_bf16 v[50:53], v[158:161], v[190:193], 0
	v_mfma_f32_16x16x32_bf16 v[46:49], v[150:153], v[198:201], 0
	v_mfma_f32_16x16x32_bf16 v[42:45], v[158:161], v[198:201], 0
	v_mfma_f32_16x16x32_bf16 v[38:41], v[150:153], v[206:209], 0
	v_mfma_f32_16x16x32_bf16 v[34:37], v[158:161], v[206:209], 0
	v_mfma_f32_16x16x32_bf16 v[94:97], v[154:157], v[186:189], v[94:97]
	v_mfma_f32_16x16x32_bf16 v[86:89], v[162:165], v[186:189], v[86:89]
	v_mfma_f32_16x16x32_bf16 v[66:69], v[154:157], v[194:197], v[66:69]
	v_mfma_f32_16x16x32_bf16 v[50:53], v[162:165], v[194:197], v[50:53]
	v_mfma_f32_16x16x32_bf16 v[46:49], v[154:157], v[202:205], v[46:49]
	v_mfma_f32_16x16x32_bf16 v[42:45], v[162:165], v[202:205], v[42:45]
	v_mfma_f32_16x16x32_bf16 v[38:41], v[154:157], v[210:213], v[38:41]
	v_mfma_f32_16x16x32_bf16 v[34:37], v[162:165], v[210:213], v[34:37]
	s_setprio 0
	s_setprio 1
	v_mfma_f32_16x16x32_bf16 v[126:129], v[166:169], v[182:185], 0
	v_mfma_f32_16x16x32_bf16 v[122:125], v[174:177], v[182:185], 0
	v_mfma_f32_16x16x32_bf16 v[118:121], v[166:169], v[190:193], 0
	v_mfma_f32_16x16x32_bf16 v[114:117], v[174:177], v[190:193], 0
	v_mfma_f32_16x16x32_bf16 v[110:113], v[166:169], v[198:201], 0
	v_mfma_f32_16x16x32_bf16 v[106:109], v[174:177], v[198:201], 0
	v_mfma_f32_16x16x32_bf16 v[102:105], v[166:169], v[206:209], 0
	v_mfma_f32_16x16x32_bf16 v[98:101], v[174:177], v[206:209], 0
	v_mfma_f32_16x16x32_bf16 v[126:129], v[170:173], v[186:189], v[126:129]
	v_mfma_f32_16x16x32_bf16 v[122:125], v[178:181], v[186:189], v[122:125]
	v_mfma_f32_16x16x32_bf16 v[118:121], v[170:173], v[194:197], v[118:121]
	v_mfma_f32_16x16x32_bf16 v[114:117], v[178:181], v[194:197], v[114:117]
	v_mfma_f32_16x16x32_bf16 v[110:113], v[170:173], v[202:205], v[110:113]
	v_mfma_f32_16x16x32_bf16 v[106:109], v[178:181], v[202:205], v[106:109]
	v_mfma_f32_16x16x32_bf16 v[102:105], v[170:173], v[210:213], v[102:105]
	v_mfma_f32_16x16x32_bf16 v[98:101], v[178:181], v[210:213], v[98:101]
	s_barrier
	s_setprio 0
	s_add_i32 s60, s47, s38
	v_lshl_add_u64 v[142:143], s[30:31], 0, v[130:131]
	s_mov_b32 m0, s60
	ds_read_b128 v[182:185], v148 offset:16384
	ds_read_b128 v[186:189], v148 offset:17408
	ds_read_b128 v[190:193], v148 offset:18432
	ds_read_b128 v[194:197], v148 offset:19456
	ds_read_b128 v[198:201], v148 offset:20480
	ds_read_b128 v[202:205], v148 offset:21504
	ds_read_b128 v[206:209], v148 offset:22528
	ds_read_b128 v[210:213], v148 offset:23552
	global_load_lds_dwordx4 v[142:143], off
	s_add_i32 m0, s60, 0x2000
	s_add_u32 s60, s30, 0x80000
	v_lshl_add_u64 v[214:215], s[30:31], 0, v[132:133]
	s_addc_u32 s61, s31, 0
	s_add_i32 s62, s48, s38
	global_load_lds_dwordx4 v[214:215], off
	v_lshl_add_u64 v[216:217], s[60:61], 0, v[130:131]
	s_mov_b32 m0, s62
	v_lshl_add_u64 v[218:219], s[34:35], 0, v[132:133]
	global_load_lds_dwordx4 v[216:217], off
	v_lshl_add_u64 v[216:217], s[60:61], 0, v[132:133]
	s_add_i32 m0, s62, 0x2000
	s_nop 0
	global_load_lds_dwordx4 v[216:217], off
	v_lshl_add_u64 v[216:217], s[34:35], 0, v[130:131]
	s_mov_b32 m0, s39
	s_nop 0
	global_load_lds_dwordx4 v[216:217], off
	s_mov_b32 m0, s40
	s_nop 0
	global_load_lds_dwordx4 v[218:219], off
	s_waitcnt vmcnt(8)
	s_waitcnt lgkmcnt(0)
	s_setprio 1
	s_barrier
	v_mfma_f32_16x16x32_bf16 v[30:33], v[150:153], v[182:185], 0
	v_mfma_f32_16x16x32_bf16 v[26:29], v[158:161], v[182:185], 0
	v_mfma_f32_16x16x32_bf16 v[22:25], v[150:153], v[190:193], 0
	v_mfma_f32_16x16x32_bf16 v[18:21], v[158:161], v[190:193], 0
	v_mfma_f32_16x16x32_bf16 v[14:17], v[150:153], v[198:201], 0
	v_mfma_f32_16x16x32_bf16 v[10:13], v[158:161], v[198:201], 0
	v_mfma_f32_16x16x32_bf16 v[6:9], v[150:153], v[206:209], 0
	v_mfma_f32_16x16x32_bf16 v[2:5], v[158:161], v[206:209], 0
	v_mfma_f32_16x16x32_bf16 v[30:33], v[154:157], v[186:189], v[30:33]
	v_mfma_f32_16x16x32_bf16 v[26:29], v[162:165], v[186:189], v[26:29]
	v_mfma_f32_16x16x32_bf16 v[22:25], v[154:157], v[194:197], v[22:25]
	v_mfma_f32_16x16x32_bf16 v[18:21], v[162:165], v[194:197], v[18:21]
	v_mfma_f32_16x16x32_bf16 v[14:17], v[154:157], v[202:205], v[14:17]
	v_mfma_f32_16x16x32_bf16 v[10:13], v[162:165], v[202:205], v[10:13]
	v_mfma_f32_16x16x32_bf16 v[6:9], v[154:157], v[210:213], v[6:9]
	v_mfma_f32_16x16x32_bf16 v[2:5], v[162:165], v[210:213], v[2:5]
	s_setprio 0
	s_setprio 1
	v_mfma_f32_16x16x32_bf16 v[90:93], v[166:169], v[182:185], 0
	v_mfma_f32_16x16x32_bf16 v[82:85], v[174:177], v[182:185], 0
	v_mfma_f32_16x16x32_bf16 v[78:81], v[166:169], v[190:193], 0
	v_mfma_f32_16x16x32_bf16 v[74:77], v[174:177], v[190:193], 0
	v_mfma_f32_16x16x32_bf16 v[70:73], v[166:169], v[198:201], 0
	v_mfma_f32_16x16x32_bf16 v[62:65], v[174:177], v[198:201], 0
	v_mfma_f32_16x16x32_bf16 v[58:61], v[166:169], v[206:209], 0
	v_mfma_f32_16x16x32_bf16 v[54:57], v[174:177], v[206:209], 0
	v_mfma_f32_16x16x32_bf16 v[90:93], v[170:173], v[186:189], v[90:93]
	v_mfma_f32_16x16x32_bf16 v[82:85], v[178:181], v[186:189], v[82:85]
	v_mfma_f32_16x16x32_bf16 v[78:81], v[170:173], v[194:197], v[78:81]
	v_mfma_f32_16x16x32_bf16 v[74:77], v[178:181], v[194:197], v[74:77]
	v_mfma_f32_16x16x32_bf16 v[70:73], v[170:173], v[202:205], v[70:73]
	v_mfma_f32_16x16x32_bf16 v[62:65], v[178:181], v[202:205], v[62:65]
	v_mfma_f32_16x16x32_bf16 v[58:61], v[170:173], v[210:213], v[58:61]
	v_mfma_f32_16x16x32_bf16 v[54:57], v[178:181], v[210:213], v[54:57]
	s_barrier
	s_setprio 0
	s_add_i32 s60, 0, 0x18000
	v_add_u32_e32 v134, s60, v144
	s_add_i32 s61, 0, 0x1c000
	ds_read_b128 v[150:153], v134
	ds_read_b128 v[154:157], v134 offset:1024
	ds_read_b128 v[158:161], v134 offset:2048
	ds_read_b128 v[162:165], v134 offset:3072
	v_add_u32_e32 v134, s61, v144
	ds_read_b128 v[166:169], v134
	ds_read_b128 v[170:173], v134 offset:1024
	ds_read_b128 v[174:177], v134 offset:2048
	ds_read_b128 v[178:181], v134 offset:3072
	s_add_u32 s34, s34, 0x80000
	s_addc_u32 s35, s35, 0
	s_mov_b32 m0, s41
	v_lshl_add_u64 v[220:221], s[34:35], 0, v[130:131]
	ds_read_b128 v[182:185], v148 offset:32768
	ds_read_b128 v[186:189], v148 offset:33792
	ds_read_b128 v[190:193], v148 offset:34816
	ds_read_b128 v[194:197], v148 offset:35840
	ds_read_b128 v[198:201], v148 offset:36864
	ds_read_b128 v[202:205], v148 offset:37888
	ds_read_b128 v[206:209], v148 offset:38912
	ds_read_b128 v[210:213], v148 offset:39936
	global_load_lds_dwordx4 v[220:221], off
	v_lshl_add_u64 v[220:221], s[34:35], 0, v[132:133]
	s_mov_b32 m0, s42
	s_nop 0
	global_load_lds_dwordx4 v[220:221], off
	s_waitcnt vmcnt(8)
	s_waitcnt lgkmcnt(0)
	s_setprio 1
	s_barrier
	v_mfma_f32_16x16x32_bf16 v[94:97], v[150:153], v[182:185], v[94:97]
	v_mfma_f32_16x16x32_bf16 v[86:89], v[158:161], v[182:185], v[86:89]
	v_mfma_f32_16x16x32_bf16 v[66:69], v[150:153], v[190:193], v[66:69]
	v_mfma_f32_16x16x32_bf16 v[50:53], v[158:161], v[190:193], v[50:53]
	v_mfma_f32_16x16x32_bf16 v[46:49], v[150:153], v[198:201], v[46:49]
	v_mfma_f32_16x16x32_bf16 v[42:45], v[158:161], v[198:201], v[42:45]
	v_mfma_f32_16x16x32_bf16 v[38:41], v[150:153], v[206:209], v[38:41]
	v_mfma_f32_16x16x32_bf16 v[34:37], v[158:161], v[206:209], v[34:37]
	v_mfma_f32_16x16x32_bf16 v[94:97], v[154:157], v[186:189], v[94:97]
	v_mfma_f32_16x16x32_bf16 v[86:89], v[162:165], v[186:189], v[86:89]
	v_mfma_f32_16x16x32_bf16 v[66:69], v[154:157], v[194:197], v[66:69]
	v_mfma_f32_16x16x32_bf16 v[50:53], v[162:165], v[194:197], v[50:53]
	v_mfma_f32_16x16x32_bf16 v[46:49], v[154:157], v[202:205], v[46:49]
	v_mfma_f32_16x16x32_bf16 v[42:45], v[162:165], v[202:205], v[42:45]
	v_mfma_f32_16x16x32_bf16 v[38:41], v[154:157], v[210:213], v[38:41]
	v_mfma_f32_16x16x32_bf16 v[34:37], v[162:165], v[210:213], v[34:37]
	s_setprio 0
	s_setprio 1
	v_mfma_f32_16x16x32_bf16 v[126:129], v[166:169], v[182:185], v[126:129]
	v_mfma_f32_16x16x32_bf16 v[122:125], v[174:177], v[182:185], v[122:125]
	v_mfma_f32_16x16x32_bf16 v[118:121], v[166:169], v[190:193], v[118:121]
	v_mfma_f32_16x16x32_bf16 v[114:117], v[174:177], v[190:193], v[114:117]
	v_mfma_f32_16x16x32_bf16 v[110:113], v[166:169], v[198:201], v[110:113]
	v_mfma_f32_16x16x32_bf16 v[106:109], v[174:177], v[198:201], v[106:109]
	v_mfma_f32_16x16x32_bf16 v[102:105], v[166:169], v[206:209], v[102:105]
	v_mfma_f32_16x16x32_bf16 v[98:101], v[174:177], v[206:209], v[98:101]
	v_mfma_f32_16x16x32_bf16 v[126:129], v[170:173], v[186:189], v[126:129]
	v_mfma_f32_16x16x32_bf16 v[122:125], v[178:181], v[186:189], v[122:125]
	v_mfma_f32_16x16x32_bf16 v[118:121], v[170:173], v[194:197], v[118:121]
	v_mfma_f32_16x16x32_bf16 v[114:117], v[178:181], v[194:197], v[114:117]
	v_mfma_f32_16x16x32_bf16 v[110:113], v[170:173], v[202:205], v[110:113]
	v_mfma_f32_16x16x32_bf16 v[106:109], v[178:181], v[202:205], v[106:109]
	v_mfma_f32_16x16x32_bf16 v[102:105], v[170:173], v[210:213], v[102:105]
	v_mfma_f32_16x16x32_bf16 v[98:101], v[178:181], v[210:213], v[98:101]
	s_barrier
	s_setprio 0
	s_add_i32 s34, s60, s38
	v_lshl_add_u64 v[142:143], v[142:143], 0, s[6:7]
	s_mov_b32 m0, s34
	ds_read_b128 v[182:185], v148 offset:49152
	ds_read_b128 v[186:189], v148 offset:50176
	ds_read_b128 v[190:193], v148 offset:51200
	ds_read_b128 v[194:197], v148 offset:52224
	ds_read_b128 v[198:201], v148 offset:53248
	ds_read_b128 v[202:205], v148 offset:54272
	ds_read_b128 v[206:209], v148 offset:55296
	ds_read_b128 v[210:213], v148 offset:56320
	global_load_lds_dwordx4 v[142:143], off
	s_add_i32 m0, s34, 0x2000
	s_add_u32 s30, s30, 0x80080
	v_lshl_add_u64 v[142:143], v[214:215], 0, s[6:7]
	s_addc_u32 s31, s31, 0
	s_add_i32 s34, s61, s38
	global_load_lds_dwordx4 v[142:143], off
	v_lshl_add_u64 v[142:143], s[30:31], 0, v[130:131]
	s_mov_b32 m0, s34
	s_nop 0
	global_load_lds_dwordx4 v[142:143], off
	v_lshl_add_u64 v[142:143], s[30:31], 0, v[132:133]
	s_add_i32 m0, s34, 0x2000
	s_nop 0
	global_load_lds_dwordx4 v[142:143], off
	v_lshl_add_u64 v[142:143], v[216:217], 0, s[6:7]
	s_mov_b32 m0, s44
	s_nop 0
	global_load_lds_dwordx4 v[142:143], off
	v_lshl_add_u64 v[142:143], v[218:219], 0, s[6:7]
	s_mov_b32 m0, s45
	s_nop 0
	global_load_lds_dwordx4 v[142:143], off
	s_waitcnt vmcnt(8)
	s_waitcnt lgkmcnt(0)
	s_setprio 1
	s_barrier
	v_mfma_f32_16x16x32_bf16 v[30:33], v[150:153], v[182:185], v[30:33]
	v_mfma_f32_16x16x32_bf16 v[26:29], v[158:161], v[182:185], v[26:29]
	v_mfma_f32_16x16x32_bf16 v[22:25], v[150:153], v[190:193], v[22:25]
	v_mfma_f32_16x16x32_bf16 v[18:21], v[158:161], v[190:193], v[18:21]
	v_mfma_f32_16x16x32_bf16 v[14:17], v[150:153], v[198:201], v[14:17]
	v_mfma_f32_16x16x32_bf16 v[10:13], v[158:161], v[198:201], v[10:13]
	v_mfma_f32_16x16x32_bf16 v[6:9], v[150:153], v[206:209], v[6:9]
	v_mfma_f32_16x16x32_bf16 v[2:5], v[158:161], v[206:209], v[2:5]
	v_mfma_f32_16x16x32_bf16 v[30:33], v[154:157], v[186:189], v[30:33]
	v_mfma_f32_16x16x32_bf16 v[26:29], v[162:165], v[186:189], v[26:29]
	v_mfma_f32_16x16x32_bf16 v[22:25], v[154:157], v[194:197], v[22:25]
	v_mfma_f32_16x16x32_bf16 v[18:21], v[162:165], v[194:197], v[18:21]
	v_mfma_f32_16x16x32_bf16 v[14:17], v[154:157], v[202:205], v[14:17]
	v_mfma_f32_16x16x32_bf16 v[10:13], v[162:165], v[202:205], v[10:13]
	v_mfma_f32_16x16x32_bf16 v[6:9], v[154:157], v[210:213], v[6:9]
	v_mfma_f32_16x16x32_bf16 v[2:5], v[162:165], v[210:213], v[2:5]
	s_setprio 0
	s_setprio 1
	v_mfma_f32_16x16x32_bf16 v[90:93], v[166:169], v[182:185], v[90:93]
	v_mfma_f32_16x16x32_bf16 v[82:85], v[174:177], v[182:185], v[82:85]
	v_mfma_f32_16x16x32_bf16 v[78:81], v[166:169], v[190:193], v[78:81]
	v_mfma_f32_16x16x32_bf16 v[74:77], v[174:177], v[190:193], v[74:77]
	v_mfma_f32_16x16x32_bf16 v[70:73], v[166:169], v[198:201], v[70:73]
	v_mfma_f32_16x16x32_bf16 v[62:65], v[174:177], v[198:201], v[62:65]
	v_mfma_f32_16x16x32_bf16 v[58:61], v[166:169], v[206:209], v[58:61]
	v_mfma_f32_16x16x32_bf16 v[54:57], v[174:177], v[206:209], v[54:57]
	v_mfma_f32_16x16x32_bf16 v[90:93], v[170:173], v[186:189], v[90:93]
	v_mfma_f32_16x16x32_bf16 v[82:85], v[178:181], v[186:189], v[82:85]
	v_mfma_f32_16x16x32_bf16 v[78:81], v[170:173], v[194:197], v[78:81]
	v_mfma_f32_16x16x32_bf16 v[74:77], v[178:181], v[194:197], v[74:77]
	v_mfma_f32_16x16x32_bf16 v[70:73], v[170:173], v[202:205], v[70:73]
	v_mfma_f32_16x16x32_bf16 v[62:65], v[178:181], v[202:205], v[62:65]
	v_mfma_f32_16x16x32_bf16 v[58:61], v[170:173], v[210:213], v[58:61]
	v_mfma_f32_16x16x32_bf16 v[54:57], v[178:181], v[210:213], v[54:57]
	s_barrier
	s_setprio 0
	s_add_i32 s59, s59, 2
	s_add_u32 s0, s0, 0x100
	s_addc_u32 s1, s1, 0
	s_add_u32 s57, s57, 0x100
	s_addc_u32 s58, s58, 0
	s_cmp_gt_u32 s59, 29

.LBB0_1345:
	s_ashr_i32 s23, s22, 31
	s_lshl_b64 s[24:25], s[22:23], 20
	v_readlane_b32 s26, v254, 22
	v_readlane_b32 s27, v254, 23
	s_add_u32 s24, s26, s24
	s_addc_u32 s25, s27, s25
	s_and_b64 s[26:27], s[8:9], exec
	s_cselect_b32 s23, s25, s31
	s_cselect_b32 s55, s24, s30
	s_ashr_i32 s21, s20, 31
	s_lshl_b64 s[26:27], s[20:21], 20
	s_add_u32 s26, s38, s26
	s_addc_u32 s27, s39, s27
	s_and_b64 s[36:37], s[8:9], exec
	s_cselect_b32 s21, s27, s35
	s_cselect_b32 s56, s26, s34
	s_add_u32 s30, s30, 0x80080
	s_addc_u32 s31, s31, 0
	s_add_u32 s57, s34, 0x100
	s_addc_u32 s58, s35, 0
	s_mov_b32 s59, -2
	ds_read_b128 v[154:157], v150
	ds_read_b128 v[158:161], v150 offset:1024
	ds_read_b128 v[162:165], v150 offset:2048
	ds_read_b128 v[166:169], v150 offset:3072
	ds_read_b128 v[170:173], v151
	ds_read_b128 v[174:177], v151 offset:1024
	ds_read_b128 v[178:181], v151 offset:2048
	ds_read_b128 v[182:185], v151 offset:3072
	s_add_u32 s34, s30, 0xfff80080
	s_addc_u32 s35, s31, -1
	s_cmp_eq_u32 s59, 28
	s_cselect_b32 s37, s23, s35
	s_cselect_b32 s36, s55, s34
	s_cselect_b32 s35, s21, s58
	s_cselect_b32 s34, s56, s57
	v_lshl_add_u64 v[146:147], s[30:31], 0, v[138:139]
	s_add_i32 m0, s29, 0xc000
	ds_read_b128 v[186:189], v152
	ds_read_b128 v[190:193], v152 offset:1024
	ds_read_b128 v[194:197], v152 offset:2048
	ds_read_b128 v[198:201], v152 offset:3072
	ds_read_b128 v[202:205], v152 offset:4096
	ds_read_b128 v[206:209], v152 offset:5120
	ds_read_b128 v[210:213], v152 offset:6144
	ds_read_b128 v[214:217], v152 offset:7168
	global_load_lds_dwordx4 v[146:147], off
	v_lshl_add_u64 v[146:147], s[30:31], 0, v[140:141]
	s_add_i32 m0, s29, 0xe000
	s_nop 0
	global_load_lds_dwordx4 v[146:147], off
	s_waitcnt vmcnt(8)
	s_waitcnt lgkmcnt(0)
	s_setprio 1
	s_barrier
	v_mfma_f32_16x16x32_bf16 v[126:129], v[154:157], v[186:189], 0
	v_mfma_f32_16x16x32_bf16 v[122:125], v[162:165], v[186:189], 0
	v_mfma_f32_16x16x32_bf16 v[118:121], v[154:157], v[194:197], 0
	v_mfma_f32_16x16x32_bf16 v[110:113], v[162:165], v[194:197], 0
	v_mfma_f32_16x16x32_bf16 v[102:105], v[154:157], v[202:205], 0
	v_mfma_f32_16x16x32_bf16 v[94:97], v[162:165], v[202:205], 0
	v_mfma_f32_16x16x32_bf16 v[86:89], v[154:157], v[210:213], 0
	v_mfma_f32_16x16x32_bf16 v[78:81], v[162:165], v[210:213], 0
	v_mfma_f32_16x16x32_bf16 v[126:129], v[158:161], v[190:193], v[126:129]
	v_mfma_f32_16x16x32_bf16 v[122:125], v[166:169], v[190:193], v[122:125]
	v_mfma_f32_16x16x32_bf16 v[118:121], v[158:161], v[198:201], v[118:121]
	v_mfma_f32_16x16x32_bf16 v[110:113], v[166:169], v[198:201], v[110:113]
	v_mfma_f32_16x16x32_bf16 v[102:105], v[158:161], v[206:209], v[102:105]
	v_mfma_f32_16x16x32_bf16 v[94:97], v[166:169], v[206:209], v[94:97]
	v_mfma_f32_16x16x32_bf16 v[86:89], v[158:161], v[214:217], v[86:89]
	v_mfma_f32_16x16x32_bf16 v[78:81], v[166:169], v[214:217], v[78:81]
	s_setprio 0
	s_setprio 1
	v_mfma_f32_16x16x32_bf16 v[114:117], v[170:173], v[186:189], 0
	v_mfma_f32_16x16x32_bf16 v[106:109], v[178:181], v[186:189], 0
	v_mfma_f32_16x16x32_bf16 v[98:101], v[170:173], v[194:197], 0
	v_mfma_f32_16x16x32_bf16 v[90:93], v[178:181], v[194:197], 0
	v_mfma_f32_16x16x32_bf16 v[82:85], v[170:173], v[202:205], 0
	v_mfma_f32_16x16x32_bf16 v[74:77], v[178:181], v[202:205], 0
	v_mfma_f32_16x16x32_bf16 v[70:73], v[170:173], v[210:213], 0
	v_mfma_f32_16x16x32_bf16 v[66:69], v[178:181], v[210:213], 0
	v_mfma_f32_16x16x32_bf16 v[114:117], v[174:177], v[190:193], v[114:117]
	v_mfma_f32_16x16x32_bf16 v[106:109], v[182:185], v[190:193], v[106:109]
	v_mfma_f32_16x16x32_bf16 v[98:101], v[174:177], v[198:201], v[98:101]
	v_mfma_f32_16x16x32_bf16 v[90:93], v[182:185], v[198:201], v[90:93]
	v_mfma_f32_16x16x32_bf16 v[82:85], v[174:177], v[206:209], v[82:85]
	v_mfma_f32_16x16x32_bf16 v[74:77], v[182:185], v[206:209], v[74:77]
	v_mfma_f32_16x16x32_bf16 v[70:73], v[174:177], v[214:217], v[70:73]
	v_mfma_f32_16x16x32_bf16 v[66:69], v[182:185], v[214:217], v[66:69]
	s_barrier
	s_setprio 0
	s_add_i32 s60, s48, s40
	v_lshl_add_u64 v[146:147], s[34:35], 0, v[132:133]
	s_mov_b32 m0, s60
	ds_read_b128 v[186:189], v152 offset:16384
	ds_read_b128 v[190:193], v152 offset:17408
	ds_read_b128 v[194:197], v152 offset:18432
	ds_read_b128 v[198:201], v152 offset:19456
	ds_read_b128 v[202:205], v152 offset:20480
	ds_read_b128 v[206:209], v152 offset:21504
	ds_read_b128 v[210:213], v152 offset:22528
	ds_read_b128 v[214:217], v152 offset:23552
	global_load_lds_dwordx4 v[146:147], off
	s_add_i32 m0, s60, 0x2000
	s_add_u32 s60, s34, 0x80000
	v_lshl_add_u64 v[218:219], s[34:35], 0, v[136:137]
	s_addc_u32 s61, s35, 0
	s_add_i32 s62, s49, s40
	global_load_lds_dwordx4 v[218:219], off
	v_lshl_add_u64 v[220:221], s[60:61], 0, v[132:133]
	s_mov_b32 m0, s62
	v_lshl_add_u64 v[222:223], s[36:37], 0, v[134:135]
	global_load_lds_dwordx4 v[220:221], off
	v_lshl_add_u64 v[220:221], s[60:61], 0, v[136:137]
	s_add_i32 m0, s62, 0x2000
	s_nop 0
	global_load_lds_dwordx4 v[220:221], off
	v_lshl_add_u64 v[220:221], s[36:37], 0, v[130:131]
	s_mov_b32 m0, s29
	s_nop 0
	global_load_lds_dwordx4 v[220:221], off
	s_mov_b32 m0, s41
	s_nop 0
	global_load_lds_dwordx4 v[222:223], off
	s_waitcnt vmcnt(8)
	s_waitcnt lgkmcnt(0)
	s_setprio 1
	s_barrier
	v_mfma_f32_16x16x32_bf16 v[62:65], v[154:157], v[186:189], 0
	v_mfma_f32_16x16x32_bf16 v[58:61], v[162:165], v[186:189], 0
	v_mfma_f32_16x16x32_bf16 v[54:57], v[154:157], v[194:197], 0
	v_mfma_f32_16x16x32_bf16 v[46:49], v[162:165], v[194:197], 0
	v_mfma_f32_16x16x32_bf16 v[38:41], v[154:157], v[202:205], 0
	v_mfma_f32_16x16x32_bf16 v[30:33], v[162:165], v[202:205], 0
	v_mfma_f32_16x16x32_bf16 v[22:25], v[154:157], v[210:213], 0
	v_mfma_f32_16x16x32_bf16 v[14:17], v[162:165], v[210:213], 0
	v_mfma_f32_16x16x32_bf16 v[62:65], v[158:161], v[190:193], v[62:65]
	v_mfma_f32_16x16x32_bf16 v[58:61], v[166:169], v[190:193], v[58:61]
	v_mfma_f32_16x16x32_bf16 v[54:57], v[158:161], v[198:201], v[54:57]
	v_mfma_f32_16x16x32_bf16 v[46:49], v[166:169], v[198:201], v[46:49]
	v_mfma_f32_16x16x32_bf16 v[38:41], v[158:161], v[206:209], v[38:41]
	v_mfma_f32_16x16x32_bf16 v[30:33], v[166:169], v[206:209], v[30:33]
	v_mfma_f32_16x16x32_bf16 v[22:25], v[158:161], v[214:217], v[22:25]
	v_mfma_f32_16x16x32_bf16 v[14:17], v[166:169], v[214:217], v[14:17]
	s_setprio 0
	s_setprio 1
	v_mfma_f32_16x16x32_bf16 v[50:53], v[170:173], v[186:189], 0
	v_mfma_f32_16x16x32_bf16 v[42:45], v[178:181], v[186:189], 0
	v_mfma_f32_16x16x32_bf16 v[34:37], v[170:173], v[194:197], 0
	v_mfma_f32_16x16x32_bf16 v[26:29], v[178:181], v[194:197], 0
	v_mfma_f32_16x16x32_bf16 v[18:21], v[170:173], v[202:205], 0
	v_mfma_f32_16x16x32_bf16 v[10:13], v[178:181], v[202:205], 0
	v_mfma_f32_16x16x32_bf16 v[6:9], v[170:173], v[210:213], 0
	v_mfma_f32_16x16x32_bf16 v[2:5], v[178:181], v[210:213], 0
	v_mfma_f32_16x16x32_bf16 v[50:53], v[174:177], v[190:193], v[50:53]
	v_mfma_f32_16x16x32_bf16 v[42:45], v[182:185], v[190:193], v[42:45]
	v_mfma_f32_16x16x32_bf16 v[34:37], v[174:177], v[198:201], v[34:37]
	v_mfma_f32_16x16x32_bf16 v[26:29], v[182:185], v[198:201], v[26:29]
	v_mfma_f32_16x16x32_bf16 v[18:21], v[174:177], v[206:209], v[18:21]
	v_mfma_f32_16x16x32_bf16 v[10:13], v[182:185], v[206:209], v[10:13]
	v_mfma_f32_16x16x32_bf16 v[6:9], v[174:177], v[214:217], v[6:9]
	v_mfma_f32_16x16x32_bf16 v[2:5], v[182:185], v[214:217], v[2:5]
	s_barrier
	s_setprio 0
	s_add_i32 s60, 0, 0x18000
	v_add_u32_e32 v153, s60, v148
	s_add_i32 s61, 0, 0x1c000
	ds_read_b128 v[154:157], v153
	ds_read_b128 v[158:161], v153 offset:1024
	ds_read_b128 v[162:165], v153 offset:2048
	ds_read_b128 v[166:169], v153 offset:3072
	v_add_u32_e32 v153, s61, v148
	ds_read_b128 v[170:173], v153
	ds_read_b128 v[174:177], v153 offset:1024
	ds_read_b128 v[178:181], v153 offset:2048
	ds_read_b128 v[182:185], v153 offset:3072
	s_add_u32 s36, s36, 0x80000
	s_addc_u32 s37, s37, 0
	s_mov_b32 m0, s42
	v_lshl_add_u64 v[224:225], s[36:37], 0, v[130:131]
	ds_read_b128 v[186:189], v152 offset:32768
	ds_read_b128 v[190:193], v152 offset:33792
	ds_read_b128 v[194:197], v152 offset:34816
	ds_read_b128 v[198:201], v152 offset:35840
	ds_read_b128 v[202:205], v152 offset:36864
	ds_read_b128 v[206:209], v152 offset:37888
	ds_read_b128 v[210:213], v152 offset:38912
	ds_read_b128 v[214:217], v152 offset:39936
	global_load_lds_dwordx4 v[224:225], off
	v_lshl_add_u64 v[224:225], s[36:37], 0, v[134:135]
	s_mov_b32 m0, s43
	s_nop 0
	global_load_lds_dwordx4 v[224:225], off
	s_waitcnt vmcnt(8)
	s_waitcnt lgkmcnt(0)
	s_setprio 1
	s_barrier
	v_mfma_f32_16x16x32_bf16 v[126:129], v[154:157], v[186:189], v[126:129]
	v_mfma_f32_16x16x32_bf16 v[122:125], v[162:165], v[186:189], v[122:125]
	v_mfma_f32_16x16x32_bf16 v[118:121], v[154:157], v[194:197], v[118:121]
	v_mfma_f32_16x16x32_bf16 v[110:113], v[162:165], v[194:197], v[110:113]
	v_mfma_f32_16x16x32_bf16 v[102:105], v[154:157], v[202:205], v[102:105]
	v_mfma_f32_16x16x32_bf16 v[94:97], v[162:165], v[202:205], v[94:97]
	v_mfma_f32_16x16x32_bf16 v[86:89], v[154:157], v[210:213], v[86:89]
	v_mfma_f32_16x16x32_bf16 v[78:81], v[162:165], v[210:213], v[78:81]
	v_mfma_f32_16x16x32_bf16 v[126:129], v[158:161], v[190:193], v[126:129]
	v_mfma_f32_16x16x32_bf16 v[122:125], v[166:169], v[190:193], v[122:125]
	v_mfma_f32_16x16x32_bf16 v[118:121], v[158:161], v[198:201], v[118:121]
	v_mfma_f32_16x16x32_bf16 v[110:113], v[166:169], v[198:201], v[110:113]
	v_mfma_f32_16x16x32_bf16 v[102:105], v[158:161], v[206:209], v[102:105]
	v_mfma_f32_16x16x32_bf16 v[94:97], v[166:169], v[206:209], v[94:97]
	v_mfma_f32_16x16x32_bf16 v[86:89], v[158:161], v[214:217], v[86:89]
	v_mfma_f32_16x16x32_bf16 v[78:81], v[166:169], v[214:217], v[78:81]
	s_setprio 0
	s_setprio 1
	v_mfma_f32_16x16x32_bf16 v[114:117], v[170:173], v[186:189], v[114:117]
	v_mfma_f32_16x16x32_bf16 v[106:109], v[178:181], v[186:189], v[106:109]
	v_mfma_f32_16x16x32_bf16 v[98:101], v[170:173], v[194:197], v[98:101]
	v_mfma_f32_16x16x32_bf16 v[90:93], v[178:181], v[194:197], v[90:93]
	v_mfma_f32_16x16x32_bf16 v[82:85], v[170:173], v[202:205], v[82:85]
	v_mfma_f32_16x16x32_bf16 v[74:77], v[178:181], v[202:205], v[74:77]
	v_mfma_f32_16x16x32_bf16 v[70:73], v[170:173], v[210:213], v[70:73]
	v_mfma_f32_16x16x32_bf16 v[66:69], v[178:181], v[210:213], v[66:69]
	v_mfma_f32_16x16x32_bf16 v[114:117], v[174:177], v[190:193], v[114:117]
	v_mfma_f32_16x16x32_bf16 v[106:109], v[182:185], v[190:193], v[106:109]
	v_mfma_f32_16x16x32_bf16 v[98:101], v[174:177], v[198:201], v[98:101]
	v_mfma_f32_16x16x32_bf16 v[90:93], v[182:185], v[198:201], v[90:93]
	v_mfma_f32_16x16x32_bf16 v[82:85], v[174:177], v[206:209], v[82:85]
	v_mfma_f32_16x16x32_bf16 v[74:77], v[182:185], v[206:209], v[74:77]
	v_mfma_f32_16x16x32_bf16 v[70:73], v[174:177], v[214:217], v[70:73]
	v_mfma_f32_16x16x32_bf16 v[66:69], v[182:185], v[214:217], v[66:69]
	s_barrier
	s_setprio 0
	s_add_i32 s36, s60, s40
	v_lshl_add_u64 v[146:147], v[146:147], 0, s[10:11]
	s_mov_b32 m0, s36
	ds_read_b128 v[186:189], v152 offset:49152
	ds_read_b128 v[190:193], v152 offset:50176
	ds_read_b128 v[194:197], v152 offset:51200
	ds_read_b128 v[198:201], v152 offset:52224
	ds_read_b128 v[202:205], v152 offset:53248
	ds_read_b128 v[206:209], v152 offset:54272
	ds_read_b128 v[210:213], v152 offset:55296
	ds_read_b128 v[214:217], v152 offset:56320
	global_load_lds_dwordx4 v[146:147], off
	s_add_i32 m0, s36, 0x2000
	s_add_u32 s34, s34, 0x80080
	v_lshl_add_u64 v[146:147], v[218:219], 0, s[10:11]
	s_addc_u32 s35, s35, 0
	s_add_i32 s36, s61, s40
	global_load_lds_dwordx4 v[146:147], off
	v_lshl_add_u64 v[146:147], s[34:35], 0, v[132:133]
	s_mov_b32 m0, s36
	s_nop 0
	global_load_lds_dwordx4 v[146:147], off
	v_lshl_add_u64 v[146:147], s[34:35], 0, v[136:137]
	s_add_i32 m0, s36, 0x2000
	s_nop 0
	global_load_lds_dwordx4 v[146:147], off
	v_lshl_add_u64 v[146:147], v[220:221], 0, s[10:11]
	s_mov_b32 m0, s45
	s_nop 0
	global_load_lds_dwordx4 v[146:147], off
	v_lshl_add_u64 v[146:147], v[222:223], 0, s[10:11]
	s_mov_b32 m0, s46
	s_nop 0
	global_load_lds_dwordx4 v[146:147], off
	s_waitcnt vmcnt(8)
	s_waitcnt lgkmcnt(0)
	s_setprio 1
	s_barrier
	v_mfma_f32_16x16x32_bf16 v[62:65], v[154:157], v[186:189], v[62:65]
	v_mfma_f32_16x16x32_bf16 v[58:61], v[162:165], v[186:189], v[58:61]
	v_mfma_f32_16x16x32_bf16 v[54:57], v[154:157], v[194:197], v[54:57]
	v_mfma_f32_16x16x32_bf16 v[46:49], v[162:165], v[194:197], v[46:49]
	v_mfma_f32_16x16x32_bf16 v[38:41], v[154:157], v[202:205], v[38:41]
	v_mfma_f32_16x16x32_bf16 v[30:33], v[162:165], v[202:205], v[30:33]
	v_mfma_f32_16x16x32_bf16 v[22:25], v[154:157], v[210:213], v[22:25]
	v_mfma_f32_16x16x32_bf16 v[14:17], v[162:165], v[210:213], v[14:17]
	v_mfma_f32_16x16x32_bf16 v[62:65], v[158:161], v[190:193], v[62:65]
	v_mfma_f32_16x16x32_bf16 v[58:61], v[166:169], v[190:193], v[58:61]
	v_mfma_f32_16x16x32_bf16 v[54:57], v[158:161], v[198:201], v[54:57]
	v_mfma_f32_16x16x32_bf16 v[46:49], v[166:169], v[198:201], v[46:49]
	v_mfma_f32_16x16x32_bf16 v[38:41], v[158:161], v[206:209], v[38:41]
	v_mfma_f32_16x16x32_bf16 v[30:33], v[166:169], v[206:209], v[30:33]
	v_mfma_f32_16x16x32_bf16 v[22:25], v[158:161], v[214:217], v[22:25]
	v_mfma_f32_16x16x32_bf16 v[14:17], v[166:169], v[214:217], v[14:17]
	s_setprio 0
	s_setprio 1
	v_mfma_f32_16x16x32_bf16 v[50:53], v[170:173], v[186:189], v[50:53]
	v_mfma_f32_16x16x32_bf16 v[42:45], v[178:181], v[186:189], v[42:45]
	v_mfma_f32_16x16x32_bf16 v[34:37], v[170:173], v[194:197], v[34:37]
	v_mfma_f32_16x16x32_bf16 v[26:29], v[178:181], v[194:197], v[26:29]
	v_mfma_f32_16x16x32_bf16 v[18:21], v[170:173], v[202:205], v[18:21]
	v_mfma_f32_16x16x32_bf16 v[10:13], v[178:181], v[202:205], v[10:13]
	v_mfma_f32_16x16x32_bf16 v[6:9], v[170:173], v[210:213], v[6:9]
	v_mfma_f32_16x16x32_bf16 v[2:5], v[178:181], v[210:213], v[2:5]
	v_mfma_f32_16x16x32_bf16 v[50:53], v[174:177], v[190:193], v[50:53]
	v_mfma_f32_16x16x32_bf16 v[42:45], v[182:185], v[190:193], v[42:45]
	v_mfma_f32_16x16x32_bf16 v[34:37], v[174:177], v[198:201], v[34:37]
	v_mfma_f32_16x16x32_bf16 v[26:29], v[182:185], v[198:201], v[26:29]
	v_mfma_f32_16x16x32_bf16 v[18:21], v[174:177], v[206:209], v[18:21]
	v_mfma_f32_16x16x32_bf16 v[10:13], v[182:185], v[206:209], v[10:13]
	v_mfma_f32_16x16x32_bf16 v[6:9], v[174:177], v[214:217], v[6:9]
	v_mfma_f32_16x16x32_bf16 v[2:5], v[182:185], v[214:217], v[2:5]
	s_barrier
	s_setprio 0
	s_add_i32 s59, s59, 2
	s_add_u32 s30, s30, 0x100
	s_addc_u32 s31, s31, 0
	s_add_u32 s57, s57, 0x100
	s_addc_u32 s58, s58, 0
	s_cmp_gt_u32 s59, 29

.LBB0_1478:
	s_ashr_i32 s19, s18, 31
	s_lshl_b64 s[22:23], s[18:19], 20
	s_add_u32 s22, s20, s22
	s_addc_u32 s23, s21, s23
	s_and_b64 s[24:25], s[8:9], exec
	s_cselect_b32 s19, s23, s29
	s_cselect_b32 s27, s22, s28
	s_ashr_i32 s17, s16, 31
	s_lshl_b64 s[24:25], s[16:17], 20
	s_add_u32 s24, s15, s24
	s_addc_u32 s25, s33, s25
	s_and_b64 s[34:35], s[8:9], exec
	s_cselect_b32 s17, s25, s31
	s_cselect_b32 s51, s24, s30
	s_add_u32 s28, s28, 0x80080
	s_addc_u32 s29, s29, 0
	s_add_u32 s52, s30, 0x100
	s_addc_u32 s53, s31, 0
	s_mov_b32 s54, -2
	s_waitcnt vmcnt(0)
	ds_read_b128 v[154:157], v150
	ds_read_b128 v[158:161], v150 offset:1024
	ds_read_b128 v[162:165], v150 offset:2048
	ds_read_b128 v[166:169], v150 offset:3072
	ds_read_b128 v[170:173], v151
	ds_read_b128 v[174:177], v151 offset:1024
	ds_read_b128 v[178:181], v151 offset:2048
	ds_read_b128 v[182:185], v151 offset:3072
	s_add_u32 s30, s28, 0xfff80080
	s_addc_u32 s31, s29, -1
	s_cmp_eq_u32 s54, 28
	s_cselect_b32 s35, s19, s31
	s_cselect_b32 s34, s27, s30
	s_cselect_b32 s31, s17, s53
	s_cselect_b32 s30, s51, s52
	v_lshl_add_u64 v[218:219], s[28:29], 0, v[140:141]
	s_add_i32 m0, s39, 0xc000
	ds_read_b128 v[186:189], v152
	ds_read_b128 v[190:193], v152 offset:1024
	ds_read_b128 v[194:197], v152 offset:2048
	ds_read_b128 v[198:201], v152 offset:3072
	ds_read_b128 v[202:205], v152 offset:4096
	ds_read_b128 v[206:209], v152 offset:5120
	ds_read_b128 v[210:213], v152 offset:6144
	ds_read_b128 v[214:217], v152 offset:7168
	global_load_lds_dwordx4 v[218:219], off
	v_lshl_add_u64 v[218:219], s[28:29], 0, v[142:143]
	s_add_i32 m0, s39, 0xe000
	s_nop 0
	global_load_lds_dwordx4 v[218:219], off
	s_waitcnt vmcnt(8)
	s_waitcnt lgkmcnt(0)
	s_setprio 1
	s_barrier
	v_mfma_f32_16x16x32_bf16 v[126:129], v[154:157], v[186:189], 0
	v_mfma_f32_16x16x32_bf16 v[122:125], v[162:165], v[186:189], 0
	v_mfma_f32_16x16x32_bf16 v[118:121], v[154:157], v[194:197], 0
	v_mfma_f32_16x16x32_bf16 v[114:117], v[162:165], v[194:197], 0
	v_mfma_f32_16x16x32_bf16 v[110:113], v[154:157], v[202:205], 0
	v_mfma_f32_16x16x32_bf16 v[102:105], v[162:165], v[202:205], 0
	v_mfma_f32_16x16x32_bf16 v[94:97], v[154:157], v[210:213], 0
	v_mfma_f32_16x16x32_bf16 v[86:89], v[162:165], v[210:213], 0
	v_mfma_f32_16x16x32_bf16 v[126:129], v[158:161], v[190:193], v[126:129]
	v_mfma_f32_16x16x32_bf16 v[122:125], v[166:169], v[190:193], v[122:125]
	v_mfma_f32_16x16x32_bf16 v[118:121], v[158:161], v[198:201], v[118:121]
	v_mfma_f32_16x16x32_bf16 v[114:117], v[166:169], v[198:201], v[114:117]
	v_mfma_f32_16x16x32_bf16 v[110:113], v[158:161], v[206:209], v[110:113]
	v_mfma_f32_16x16x32_bf16 v[102:105], v[166:169], v[206:209], v[102:105]
	v_mfma_f32_16x16x32_bf16 v[94:97], v[158:161], v[214:217], v[94:97]
	v_mfma_f32_16x16x32_bf16 v[86:89], v[166:169], v[214:217], v[86:89]
	s_setprio 0
	s_setprio 1
	v_mfma_f32_16x16x32_bf16 v[106:109], v[170:173], v[186:189], 0
	v_mfma_f32_16x16x32_bf16 v[98:101], v[178:181], v[186:189], 0
	v_mfma_f32_16x16x32_bf16 v[90:93], v[170:173], v[194:197], 0
	v_mfma_f32_16x16x32_bf16 v[82:85], v[178:181], v[194:197], 0
	v_mfma_f32_16x16x32_bf16 v[78:81], v[170:173], v[202:205], 0
	v_mfma_f32_16x16x32_bf16 v[74:77], v[178:181], v[202:205], 0
	v_mfma_f32_16x16x32_bf16 v[70:73], v[170:173], v[210:213], 0
	v_mfma_f32_16x16x32_bf16 v[66:69], v[178:181], v[210:213], 0
	v_mfma_f32_16x16x32_bf16 v[106:109], v[174:177], v[190:193], v[106:109]
	v_mfma_f32_16x16x32_bf16 v[98:101], v[182:185], v[190:193], v[98:101]
	v_mfma_f32_16x16x32_bf16 v[90:93], v[174:177], v[198:201], v[90:93]
	v_mfma_f32_16x16x32_bf16 v[82:85], v[182:185], v[198:201], v[82:85]
	v_mfma_f32_16x16x32_bf16 v[78:81], v[174:177], v[206:209], v[78:81]
	v_mfma_f32_16x16x32_bf16 v[74:77], v[182:185], v[206:209], v[74:77]
	v_mfma_f32_16x16x32_bf16 v[70:73], v[174:177], v[214:217], v[70:73]
	v_mfma_f32_16x16x32_bf16 v[66:69], v[182:185], v[214:217], v[66:69]
	s_barrier
	s_setprio 0
	s_add_i32 s55, s47, s36
	v_lshl_add_u64 v[218:219], s[30:31], 0, v[134:135]
	s_mov_b32 m0, s55
	ds_read_b128 v[186:189], v152 offset:16384
	ds_read_b128 v[190:193], v152 offset:17408
	ds_read_b128 v[194:197], v152 offset:18432
	ds_read_b128 v[198:201], v152 offset:19456
	ds_read_b128 v[202:205], v152 offset:20480
	ds_read_b128 v[206:209], v152 offset:21504
	ds_read_b128 v[210:213], v152 offset:22528
	ds_read_b128 v[214:217], v152 offset:23552
	global_load_lds_dwordx4 v[218:219], off
	s_add_i32 m0, s55, 0x2000
	s_add_u32 s56, s30, 0x80000
	v_lshl_add_u64 v[220:221], s[30:31], 0, v[130:131]
	s_addc_u32 s57, s31, 0
	s_add_i32 s55, s48, s36
	global_load_lds_dwordx4 v[220:221], off
	v_lshl_add_u64 v[222:223], s[56:57], 0, v[134:135]
	s_mov_b32 m0, s55
	v_lshl_add_u64 v[224:225], s[34:35], 0, v[132:133]
	global_load_lds_dwordx4 v[222:223], off
	v_lshl_add_u64 v[222:223], s[56:57], 0, v[130:131]
	s_add_i32 m0, s55, 0x2000
	s_nop 0
	global_load_lds_dwordx4 v[222:223], off
	v_lshl_add_u64 v[222:223], s[34:35], 0, v[136:137]
	s_mov_b32 m0, s39
	s_nop 0
	global_load_lds_dwordx4 v[222:223], off
	s_mov_b32 m0, s40
	s_nop 0
	global_load_lds_dwordx4 v[224:225], off
	s_waitcnt vmcnt(8)
	s_waitcnt lgkmcnt(0)
	s_setprio 1
	s_barrier
	v_mfma_f32_16x16x32_bf16 v[62:65], v[154:157], v[186:189], 0
	v_mfma_f32_16x16x32_bf16 v[58:61], v[162:165], v[186:189], 0
	v_mfma_f32_16x16x32_bf16 v[54:57], v[154:157], v[194:197], 0
	v_mfma_f32_16x16x32_bf16 v[50:53], v[162:165], v[194:197], 0
	v_mfma_f32_16x16x32_bf16 v[46:49], v[154:157], v[202:205], 0
	v_mfma_f32_16x16x32_bf16 v[38:41], v[162:165], v[202:205], 0
	v_mfma_f32_16x16x32_bf16 v[30:33], v[154:157], v[210:213], 0
	v_mfma_f32_16x16x32_bf16 v[22:25], v[162:165], v[210:213], 0
	v_mfma_f32_16x16x32_bf16 v[62:65], v[158:161], v[190:193], v[62:65]
	v_mfma_f32_16x16x32_bf16 v[58:61], v[166:169], v[190:193], v[58:61]
	v_mfma_f32_16x16x32_bf16 v[54:57], v[158:161], v[198:201], v[54:57]
	v_mfma_f32_16x16x32_bf16 v[50:53], v[166:169], v[198:201], v[50:53]
	v_mfma_f32_16x16x32_bf16 v[46:49], v[158:161], v[206:209], v[46:49]
	v_mfma_f32_16x16x32_bf16 v[38:41], v[166:169], v[206:209], v[38:41]
	v_mfma_f32_16x16x32_bf16 v[30:33], v[158:161], v[214:217], v[30:33]
	v_mfma_f32_16x16x32_bf16 v[22:25], v[166:169], v[214:217], v[22:25]
	s_setprio 0
	s_setprio 1
	v_mfma_f32_16x16x32_bf16 v[42:45], v[170:173], v[186:189], 0
	v_mfma_f32_16x16x32_bf16 v[34:37], v[178:181], v[186:189], 0
	v_mfma_f32_16x16x32_bf16 v[26:29], v[170:173], v[194:197], 0
	v_mfma_f32_16x16x32_bf16 v[18:21], v[178:181], v[194:197], 0
	v_mfma_f32_16x16x32_bf16 v[14:17], v[170:173], v[202:205], 0
	v_mfma_f32_16x16x32_bf16 v[10:13], v[178:181], v[202:205], 0
	v_mfma_f32_16x16x32_bf16 v[6:9], v[170:173], v[210:213], 0
	v_mfma_f32_16x16x32_bf16 v[2:5], v[178:181], v[210:213], 0
	v_mfma_f32_16x16x32_bf16 v[42:45], v[174:177], v[190:193], v[42:45]
	v_mfma_f32_16x16x32_bf16 v[34:37], v[182:185], v[190:193], v[34:37]
	v_mfma_f32_16x16x32_bf16 v[26:29], v[174:177], v[198:201], v[26:29]
	v_mfma_f32_16x16x32_bf16 v[18:21], v[182:185], v[198:201], v[18:21]
	v_mfma_f32_16x16x32_bf16 v[14:17], v[174:177], v[206:209], v[14:17]
	v_mfma_f32_16x16x32_bf16 v[10:13], v[182:185], v[206:209], v[10:13]
	v_mfma_f32_16x16x32_bf16 v[6:9], v[174:177], v[214:217], v[6:9]
	v_mfma_f32_16x16x32_bf16 v[2:5], v[182:185], v[214:217], v[2:5]
	s_barrier
	s_setprio 0
	s_add_i32 s55, 0, 0x18000
	v_add_u32_e32 v153, s55, v148
	s_add_i32 s56, 0, 0x1c000
	ds_read_b128 v[154:157], v153
	ds_read_b128 v[158:161], v153 offset:1024
	ds_read_b128 v[162:165], v153 offset:2048
	ds_read_b128 v[166:169], v153 offset:3072
	v_add_u32_e32 v153, s56, v148
	ds_read_b128 v[170:173], v153
	ds_read_b128 v[174:177], v153 offset:1024
	ds_read_b128 v[178:181], v153 offset:2048
	ds_read_b128 v[182:185], v153 offset:3072
	s_add_u32 s34, s34, 0x80000
	s_addc_u32 s35, s35, 0
	s_mov_b32 m0, s41
	v_lshl_add_u64 v[226:227], s[34:35], 0, v[136:137]
	ds_read_b128 v[186:189], v152 offset:32768
	ds_read_b128 v[190:193], v152 offset:33792
	ds_read_b128 v[194:197], v152 offset:34816
	ds_read_b128 v[198:201], v152 offset:35840
	ds_read_b128 v[202:205], v152 offset:36864
	ds_read_b128 v[206:209], v152 offset:37888
	ds_read_b128 v[210:213], v152 offset:38912
	ds_read_b128 v[214:217], v152 offset:39936
	global_load_lds_dwordx4 v[226:227], off
	v_lshl_add_u64 v[226:227], s[34:35], 0, v[132:133]
	s_mov_b32 m0, s42
	s_nop 0
	global_load_lds_dwordx4 v[226:227], off
	s_waitcnt vmcnt(8)
	s_waitcnt lgkmcnt(0)
	s_setprio 1
	s_barrier
	v_mfma_f32_16x16x32_bf16 v[126:129], v[154:157], v[186:189], v[126:129]
	v_mfma_f32_16x16x32_bf16 v[122:125], v[162:165], v[186:189], v[122:125]
	v_mfma_f32_16x16x32_bf16 v[118:121], v[154:157], v[194:197], v[118:121]
	v_mfma_f32_16x16x32_bf16 v[114:117], v[162:165], v[194:197], v[114:117]
	v_mfma_f32_16x16x32_bf16 v[110:113], v[154:157], v[202:205], v[110:113]
	v_mfma_f32_16x16x32_bf16 v[102:105], v[162:165], v[202:205], v[102:105]
	v_mfma_f32_16x16x32_bf16 v[94:97], v[154:157], v[210:213], v[94:97]
	v_mfma_f32_16x16x32_bf16 v[86:89], v[162:165], v[210:213], v[86:89]
	v_mfma_f32_16x16x32_bf16 v[126:129], v[158:161], v[190:193], v[126:129]
	v_mfma_f32_16x16x32_bf16 v[122:125], v[166:169], v[190:193], v[122:125]
	v_mfma_f32_16x16x32_bf16 v[118:121], v[158:161], v[198:201], v[118:121]
	v_mfma_f32_16x16x32_bf16 v[114:117], v[166:169], v[198:201], v[114:117]
	v_mfma_f32_16x16x32_bf16 v[110:113], v[158:161], v[206:209], v[110:113]
	v_mfma_f32_16x16x32_bf16 v[102:105], v[166:169], v[206:209], v[102:105]
	v_mfma_f32_16x16x32_bf16 v[94:97], v[158:161], v[214:217], v[94:97]
	v_mfma_f32_16x16x32_bf16 v[86:89], v[166:169], v[214:217], v[86:89]
	s_setprio 0
	s_setprio 1
	v_mfma_f32_16x16x32_bf16 v[106:109], v[170:173], v[186:189], v[106:109]
	v_mfma_f32_16x16x32_bf16 v[98:101], v[178:181], v[186:189], v[98:101]
	v_mfma_f32_16x16x32_bf16 v[90:93], v[170:173], v[194:197], v[90:93]
	v_mfma_f32_16x16x32_bf16 v[82:85], v[178:181], v[194:197], v[82:85]
	v_mfma_f32_16x16x32_bf16 v[78:81], v[170:173], v[202:205], v[78:81]
	v_mfma_f32_16x16x32_bf16 v[74:77], v[178:181], v[202:205], v[74:77]
	v_mfma_f32_16x16x32_bf16 v[70:73], v[170:173], v[210:213], v[70:73]
	v_mfma_f32_16x16x32_bf16 v[66:69], v[178:181], v[210:213], v[66:69]
	v_mfma_f32_16x16x32_bf16 v[106:109], v[174:177], v[190:193], v[106:109]
	v_mfma_f32_16x16x32_bf16 v[98:101], v[182:185], v[190:193], v[98:101]
	v_mfma_f32_16x16x32_bf16 v[90:93], v[174:177], v[198:201], v[90:93]
	v_mfma_f32_16x16x32_bf16 v[82:85], v[182:185], v[198:201], v[82:85]
	v_mfma_f32_16x16x32_bf16 v[78:81], v[174:177], v[206:209], v[78:81]
	v_mfma_f32_16x16x32_bf16 v[74:77], v[182:185], v[206:209], v[74:77]
	v_mfma_f32_16x16x32_bf16 v[70:73], v[174:177], v[214:217], v[70:73]
	v_mfma_f32_16x16x32_bf16 v[66:69], v[182:185], v[214:217], v[66:69]
	s_barrier
	s_setprio 0
	s_add_i32 s34, s55, s36
	v_lshl_add_u64 v[218:219], v[218:219], 0, s[10:11]
	s_mov_b32 m0, s34
	ds_read_b128 v[186:189], v152 offset:49152
	ds_read_b128 v[190:193], v152 offset:50176
	ds_read_b128 v[194:197], v152 offset:51200
	ds_read_b128 v[198:201], v152 offset:52224
	ds_read_b128 v[202:205], v152 offset:53248
	ds_read_b128 v[206:209], v152 offset:54272
	ds_read_b128 v[210:213], v152 offset:55296
	ds_read_b128 v[214:217], v152 offset:56320
	global_load_lds_dwordx4 v[218:219], off
	s_add_i32 m0, s34, 0x2000
	s_add_u32 s30, s30, 0x80080
	v_lshl_add_u64 v[218:219], v[220:221], 0, s[10:11]
	s_addc_u32 s31, s31, 0
	s_add_i32 s34, s56, s36
	global_load_lds_dwordx4 v[218:219], off
	v_lshl_add_u64 v[218:219], s[30:31], 0, v[134:135]
	s_mov_b32 m0, s34
	s_nop 0
	global_load_lds_dwordx4 v[218:219], off
	v_lshl_add_u64 v[218:219], s[30:31], 0, v[130:131]
	s_add_i32 m0, s34, 0x2000
	s_nop 0
	global_load_lds_dwordx4 v[218:219], off
	v_lshl_add_u64 v[218:219], v[222:223], 0, s[10:11]
	s_mov_b32 m0, s44
	s_nop 0
	global_load_lds_dwordx4 v[218:219], off
	v_lshl_add_u64 v[218:219], v[224:225], 0, s[10:11]
	s_mov_b32 m0, s45
	s_nop 0
	global_load_lds_dwordx4 v[218:219], off
	s_waitcnt vmcnt(8)
	s_waitcnt lgkmcnt(0)
	s_setprio 1
	s_barrier
	v_mfma_f32_16x16x32_bf16 v[62:65], v[154:157], v[186:189], v[62:65]
	v_mfma_f32_16x16x32_bf16 v[58:61], v[162:165], v[186:189], v[58:61]
	v_mfma_f32_16x16x32_bf16 v[54:57], v[154:157], v[194:197], v[54:57]
	v_mfma_f32_16x16x32_bf16 v[50:53], v[162:165], v[194:197], v[50:53]
	v_mfma_f32_16x16x32_bf16 v[46:49], v[154:157], v[202:205], v[46:49]
	v_mfma_f32_16x16x32_bf16 v[38:41], v[162:165], v[202:205], v[38:41]
	v_mfma_f32_16x16x32_bf16 v[30:33], v[154:157], v[210:213], v[30:33]
	v_mfma_f32_16x16x32_bf16 v[22:25], v[162:165], v[210:213], v[22:25]
	v_mfma_f32_16x16x32_bf16 v[62:65], v[158:161], v[190:193], v[62:65]
	v_mfma_f32_16x16x32_bf16 v[58:61], v[166:169], v[190:193], v[58:61]
	v_mfma_f32_16x16x32_bf16 v[54:57], v[158:161], v[198:201], v[54:57]
	v_mfma_f32_16x16x32_bf16 v[50:53], v[166:169], v[198:201], v[50:53]
	v_mfma_f32_16x16x32_bf16 v[46:49], v[158:161], v[206:209], v[46:49]
	v_mfma_f32_16x16x32_bf16 v[38:41], v[166:169], v[206:209], v[38:41]
	v_mfma_f32_16x16x32_bf16 v[30:33], v[158:161], v[214:217], v[30:33]
	v_mfma_f32_16x16x32_bf16 v[22:25], v[166:169], v[214:217], v[22:25]
	s_setprio 0
	s_setprio 1
	v_mfma_f32_16x16x32_bf16 v[42:45], v[170:173], v[186:189], v[42:45]
	v_mfma_f32_16x16x32_bf16 v[34:37], v[178:181], v[186:189], v[34:37]
	v_mfma_f32_16x16x32_bf16 v[26:29], v[170:173], v[194:197], v[26:29]
	v_mfma_f32_16x16x32_bf16 v[18:21], v[178:181], v[194:197], v[18:21]
	v_mfma_f32_16x16x32_bf16 v[14:17], v[170:173], v[202:205], v[14:17]
	v_mfma_f32_16x16x32_bf16 v[10:13], v[178:181], v[202:205], v[10:13]
	v_mfma_f32_16x16x32_bf16 v[6:9], v[170:173], v[210:213], v[6:9]
	v_mfma_f32_16x16x32_bf16 v[2:5], v[178:181], v[210:213], v[2:5]
	v_mfma_f32_16x16x32_bf16 v[42:45], v[174:177], v[190:193], v[42:45]
	v_mfma_f32_16x16x32_bf16 v[34:37], v[182:185], v[190:193], v[34:37]
	v_mfma_f32_16x16x32_bf16 v[26:29], v[174:177], v[198:201], v[26:29]
	v_mfma_f32_16x16x32_bf16 v[18:21], v[182:185], v[198:201], v[18:21]
	v_mfma_f32_16x16x32_bf16 v[14:17], v[174:177], v[206:209], v[14:17]
	v_mfma_f32_16x16x32_bf16 v[10:13], v[182:185], v[206:209], v[10:13]
	v_mfma_f32_16x16x32_bf16 v[6:9], v[174:177], v[214:217], v[6:9]
	v_mfma_f32_16x16x32_bf16 v[2:5], v[182:185], v[214:217], v[2:5]
	s_barrier
	s_setprio 0
	s_add_i32 s54, s54, 2
	s_add_u32 s28, s28, 0x100
	s_addc_u32 s29, s29, 0
	s_add_u32 s52, s52, 0x100
	s_addc_u32 s53, s53, 0
	s_cmp_gt_u32 s54, 29

.LBB0_1561:
	s_add_u32 s26, s26, 0x160080
	s_addc_u32 s27, s27, 0
	s_add_u32 s57, s28, 0x100
	s_addc_u32 s58, s29, 0
	s_mov_b32 s59, -2
	ds_read_b128 v[154:157], v150
	ds_read_b128 v[158:161], v150 offset:1024
	ds_read_b128 v[162:165], v150 offset:2048
	ds_read_b128 v[166:169], v150 offset:3072
	ds_read_b128 v[170:173], v151
	ds_read_b128 v[174:177], v151 offset:1024
	ds_read_b128 v[178:181], v151 offset:2048
	ds_read_b128 v[182:185], v151 offset:3072
	s_add_u32 s28, s26, 0xffea0080
	s_addc_u32 s29, s27, -1
	s_cmpk_eq_i32 s59, 0x54
	s_cselect_b32 s31, s1, s29
	s_cselect_b32 s30, s0, s28
	s_cselect_b32 s29, s25, s58
	s_cselect_b32 s28, s24, s57
	v_lshl_add_u64 v[146:147], s[26:27], 0, v[138:139]
	s_add_i32 m0, s39, 0xc000
	ds_read_b128 v[186:189], v152
	ds_read_b128 v[190:193], v152 offset:1024
	ds_read_b128 v[194:197], v152 offset:2048
	ds_read_b128 v[198:201], v152 offset:3072
	ds_read_b128 v[202:205], v152 offset:4096
	ds_read_b128 v[206:209], v152 offset:5120
	ds_read_b128 v[210:213], v152 offset:6144
	ds_read_b128 v[214:217], v152 offset:7168
	global_load_lds_dwordx4 v[146:147], off
	v_lshl_add_u64 v[146:147], s[26:27], 0, v[140:141]
	s_add_i32 m0, s39, 0xe000
	s_nop 0
	global_load_lds_dwordx4 v[146:147], off
	s_waitcnt vmcnt(8)
	s_waitcnt lgkmcnt(0)
	s_setprio 1
	s_barrier
	v_mfma_f32_16x16x32_bf16 v[126:129], v[154:157], v[186:189], 0
	v_mfma_f32_16x16x32_bf16 v[122:125], v[162:165], v[186:189], 0
	v_mfma_f32_16x16x32_bf16 v[118:121], v[154:157], v[194:197], 0
	v_mfma_f32_16x16x32_bf16 v[110:113], v[162:165], v[194:197], 0
	v_mfma_f32_16x16x32_bf16 v[102:105], v[154:157], v[202:205], 0
	v_mfma_f32_16x16x32_bf16 v[94:97], v[162:165], v[202:205], 0
	v_mfma_f32_16x16x32_bf16 v[86:89], v[154:157], v[210:213], 0
	v_mfma_f32_16x16x32_bf16 v[78:81], v[162:165], v[210:213], 0
	v_mfma_f32_16x16x32_bf16 v[126:129], v[158:161], v[190:193], v[126:129]
	v_mfma_f32_16x16x32_bf16 v[122:125], v[166:169], v[190:193], v[122:125]
	v_mfma_f32_16x16x32_bf16 v[118:121], v[158:161], v[198:201], v[118:121]
	v_mfma_f32_16x16x32_bf16 v[110:113], v[166:169], v[198:201], v[110:113]
	v_mfma_f32_16x16x32_bf16 v[102:105], v[158:161], v[206:209], v[102:105]
	v_mfma_f32_16x16x32_bf16 v[94:97], v[166:169], v[206:209], v[94:97]
	v_mfma_f32_16x16x32_bf16 v[86:89], v[158:161], v[214:217], v[86:89]
	v_mfma_f32_16x16x32_bf16 v[78:81], v[166:169], v[214:217], v[78:81]
	s_setprio 0
	s_setprio 1
	v_mfma_f32_16x16x32_bf16 v[114:117], v[170:173], v[186:189], 0
	v_mfma_f32_16x16x32_bf16 v[106:109], v[178:181], v[186:189], 0
	v_mfma_f32_16x16x32_bf16 v[98:101], v[170:173], v[194:197], 0
	v_mfma_f32_16x16x32_bf16 v[90:93], v[178:181], v[194:197], 0
	v_mfma_f32_16x16x32_bf16 v[82:85], v[170:173], v[202:205], 0
	v_mfma_f32_16x16x32_bf16 v[74:77], v[178:181], v[202:205], 0
	v_mfma_f32_16x16x32_bf16 v[70:73], v[170:173], v[210:213], 0
	v_mfma_f32_16x16x32_bf16 v[66:69], v[178:181], v[210:213], 0
	v_mfma_f32_16x16x32_bf16 v[114:117], v[174:177], v[190:193], v[114:117]
	v_mfma_f32_16x16x32_bf16 v[106:109], v[182:185], v[190:193], v[106:109]
	v_mfma_f32_16x16x32_bf16 v[98:101], v[174:177], v[198:201], v[98:101]
	v_mfma_f32_16x16x32_bf16 v[90:93], v[182:185], v[198:201], v[90:93]
	v_mfma_f32_16x16x32_bf16 v[82:85], v[174:177], v[206:209], v[82:85]
	v_mfma_f32_16x16x32_bf16 v[74:77], v[182:185], v[206:209], v[74:77]
	v_mfma_f32_16x16x32_bf16 v[70:73], v[174:177], v[214:217], v[70:73]
	v_mfma_f32_16x16x32_bf16 v[66:69], v[182:185], v[214:217], v[66:69]
	s_barrier
	s_setprio 0
	s_add_i32 s60, s47, s38
	v_lshl_add_u64 v[146:147], s[28:29], 0, v[132:133]
	s_mov_b32 m0, s60
	ds_read_b128 v[186:189], v152 offset:16384
	ds_read_b128 v[190:193], v152 offset:17408
	ds_read_b128 v[194:197], v152 offset:18432
	ds_read_b128 v[198:201], v152 offset:19456
	ds_read_b128 v[202:205], v152 offset:20480
	ds_read_b128 v[206:209], v152 offset:21504
	ds_read_b128 v[210:213], v152 offset:22528
	ds_read_b128 v[214:217], v152 offset:23552
	global_load_lds_dwordx4 v[146:147], off
	s_add_i32 m0, s60, 0x2000
	s_add_u32 s60, s28, 0x160000
	v_lshl_add_u64 v[218:219], s[28:29], 0, v[136:137]
	s_addc_u32 s61, s29, 0
	s_add_i32 s62, s48, s38
	global_load_lds_dwordx4 v[218:219], off
	v_lshl_add_u64 v[220:221], s[60:61], 0, v[132:133]
	s_mov_b32 m0, s62
	v_lshl_add_u64 v[222:223], s[30:31], 0, v[134:135]
	global_load_lds_dwordx4 v[220:221], off
	v_lshl_add_u64 v[220:221], s[60:61], 0, v[136:137]
	s_add_i32 m0, s62, 0x2000
	s_nop 0
	global_load_lds_dwordx4 v[220:221], off
	v_lshl_add_u64 v[220:221], s[30:31], 0, v[130:131]
	s_mov_b32 m0, s39
	s_nop 0
	global_load_lds_dwordx4 v[220:221], off
	s_mov_b32 m0, s40
	s_nop 0
	global_load_lds_dwordx4 v[222:223], off
	s_waitcnt vmcnt(8)
	s_waitcnt lgkmcnt(0)
	s_setprio 1
	s_barrier
	v_mfma_f32_16x16x32_bf16 v[62:65], v[154:157], v[186:189], 0
	v_mfma_f32_16x16x32_bf16 v[58:61], v[162:165], v[186:189], 0
	v_mfma_f32_16x16x32_bf16 v[54:57], v[154:157], v[194:197], 0
	v_mfma_f32_16x16x32_bf16 v[46:49], v[162:165], v[194:197], 0
	v_mfma_f32_16x16x32_bf16 v[38:41], v[154:157], v[202:205], 0
	v_mfma_f32_16x16x32_bf16 v[30:33], v[162:165], v[202:205], 0
	v_mfma_f32_16x16x32_bf16 v[22:25], v[154:157], v[210:213], 0
	v_mfma_f32_16x16x32_bf16 v[14:17], v[162:165], v[210:213], 0
	v_mfma_f32_16x16x32_bf16 v[62:65], v[158:161], v[190:193], v[62:65]
	v_mfma_f32_16x16x32_bf16 v[58:61], v[166:169], v[190:193], v[58:61]
	v_mfma_f32_16x16x32_bf16 v[54:57], v[158:161], v[198:201], v[54:57]
	v_mfma_f32_16x16x32_bf16 v[46:49], v[166:169], v[198:201], v[46:49]
	v_mfma_f32_16x16x32_bf16 v[38:41], v[158:161], v[206:209], v[38:41]
	v_mfma_f32_16x16x32_bf16 v[30:33], v[166:169], v[206:209], v[30:33]
	v_mfma_f32_16x16x32_bf16 v[22:25], v[158:161], v[214:217], v[22:25]
	v_mfma_f32_16x16x32_bf16 v[14:17], v[166:169], v[214:217], v[14:17]
	s_setprio 0
	s_setprio 1
	v_mfma_f32_16x16x32_bf16 v[50:53], v[170:173], v[186:189], 0
	v_mfma_f32_16x16x32_bf16 v[42:45], v[178:181], v[186:189], 0
	v_mfma_f32_16x16x32_bf16 v[34:37], v[170:173], v[194:197], 0
	v_mfma_f32_16x16x32_bf16 v[26:29], v[178:181], v[194:197], 0
	v_mfma_f32_16x16x32_bf16 v[18:21], v[170:173], v[202:205], 0
	v_mfma_f32_16x16x32_bf16 v[10:13], v[178:181], v[202:205], 0
	v_mfma_f32_16x16x32_bf16 v[6:9], v[170:173], v[210:213], 0
	v_mfma_f32_16x16x32_bf16 v[2:5], v[178:181], v[210:213], 0
	v_mfma_f32_16x16x32_bf16 v[50:53], v[174:177], v[190:193], v[50:53]
	v_mfma_f32_16x16x32_bf16 v[42:45], v[182:185], v[190:193], v[42:45]
	v_mfma_f32_16x16x32_bf16 v[34:37], v[174:177], v[198:201], v[34:37]
	v_mfma_f32_16x16x32_bf16 v[26:29], v[182:185], v[198:201], v[26:29]
	v_mfma_f32_16x16x32_bf16 v[18:21], v[174:177], v[206:209], v[18:21]
	v_mfma_f32_16x16x32_bf16 v[10:13], v[182:185], v[206:209], v[10:13]
	v_mfma_f32_16x16x32_bf16 v[6:9], v[174:177], v[214:217], v[6:9]
	v_mfma_f32_16x16x32_bf16 v[2:5], v[182:185], v[214:217], v[2:5]
	s_barrier
	s_setprio 0
	s_add_i32 s60, 0, 0x18000
	v_add_u32_e32 v153, s60, v148
	s_add_i32 s61, 0, 0x1c000
	ds_read_b128 v[154:157], v153
	ds_read_b128 v[158:161], v153 offset:1024
	ds_read_b128 v[162:165], v153 offset:2048
	ds_read_b128 v[166:169], v153 offset:3072
	v_add_u32_e32 v153, s61, v148
	ds_read_b128 v[170:173], v153
	ds_read_b128 v[174:177], v153 offset:1024
	ds_read_b128 v[178:181], v153 offset:2048
	ds_read_b128 v[182:185], v153 offset:3072
	s_add_u32 s30, s30, 0x160000
	s_addc_u32 s31, s31, 0
	s_mov_b32 m0, s41
	v_lshl_add_u64 v[224:225], s[30:31], 0, v[130:131]
	ds_read_b128 v[186:189], v152 offset:32768
	ds_read_b128 v[190:193], v152 offset:33792
	ds_read_b128 v[194:197], v152 offset:34816
	ds_read_b128 v[198:201], v152 offset:35840
	ds_read_b128 v[202:205], v152 offset:36864
	ds_read_b128 v[206:209], v152 offset:37888
	ds_read_b128 v[210:213], v152 offset:38912
	ds_read_b128 v[214:217], v152 offset:39936
	global_load_lds_dwordx4 v[224:225], off
	v_lshl_add_u64 v[224:225], s[30:31], 0, v[134:135]
	s_mov_b32 m0, s42
	s_nop 0
	global_load_lds_dwordx4 v[224:225], off
	s_waitcnt vmcnt(8)
	s_waitcnt lgkmcnt(0)
	s_setprio 1
	s_barrier
	v_mfma_f32_16x16x32_bf16 v[126:129], v[154:157], v[186:189], v[126:129]
	v_mfma_f32_16x16x32_bf16 v[122:125], v[162:165], v[186:189], v[122:125]
	v_mfma_f32_16x16x32_bf16 v[118:121], v[154:157], v[194:197], v[118:121]
	v_mfma_f32_16x16x32_bf16 v[110:113], v[162:165], v[194:197], v[110:113]
	v_mfma_f32_16x16x32_bf16 v[102:105], v[154:157], v[202:205], v[102:105]
	v_mfma_f32_16x16x32_bf16 v[94:97], v[162:165], v[202:205], v[94:97]
	v_mfma_f32_16x16x32_bf16 v[86:89], v[154:157], v[210:213], v[86:89]
	v_mfma_f32_16x16x32_bf16 v[78:81], v[162:165], v[210:213], v[78:81]
	v_mfma_f32_16x16x32_bf16 v[126:129], v[158:161], v[190:193], v[126:129]
	v_mfma_f32_16x16x32_bf16 v[122:125], v[166:169], v[190:193], v[122:125]
	v_mfma_f32_16x16x32_bf16 v[118:121], v[158:161], v[198:201], v[118:121]
	v_mfma_f32_16x16x32_bf16 v[110:113], v[166:169], v[198:201], v[110:113]
	v_mfma_f32_16x16x32_bf16 v[102:105], v[158:161], v[206:209], v[102:105]
	v_mfma_f32_16x16x32_bf16 v[94:97], v[166:169], v[206:209], v[94:97]
	v_mfma_f32_16x16x32_bf16 v[86:89], v[158:161], v[214:217], v[86:89]
	v_mfma_f32_16x16x32_bf16 v[78:81], v[166:169], v[214:217], v[78:81]
	s_setprio 0
	s_setprio 1
	v_mfma_f32_16x16x32_bf16 v[114:117], v[170:173], v[186:189], v[114:117]
	v_mfma_f32_16x16x32_bf16 v[106:109], v[178:181], v[186:189], v[106:109]
	v_mfma_f32_16x16x32_bf16 v[98:101], v[170:173], v[194:197], v[98:101]
	v_mfma_f32_16x16x32_bf16 v[90:93], v[178:181], v[194:197], v[90:93]
	v_mfma_f32_16x16x32_bf16 v[82:85], v[170:173], v[202:205], v[82:85]
	v_mfma_f32_16x16x32_bf16 v[74:77], v[178:181], v[202:205], v[74:77]
	v_mfma_f32_16x16x32_bf16 v[70:73], v[170:173], v[210:213], v[70:73]
	v_mfma_f32_16x16x32_bf16 v[66:69], v[178:181], v[210:213], v[66:69]
	v_mfma_f32_16x16x32_bf16 v[114:117], v[174:177], v[190:193], v[114:117]
	v_mfma_f32_16x16x32_bf16 v[106:109], v[182:185], v[190:193], v[106:109]
	v_mfma_f32_16x16x32_bf16 v[98:101], v[174:177], v[198:201], v[98:101]
	v_mfma_f32_16x16x32_bf16 v[90:93], v[182:185], v[198:201], v[90:93]
	v_mfma_f32_16x16x32_bf16 v[82:85], v[174:177], v[206:209], v[82:85]
	v_mfma_f32_16x16x32_bf16 v[74:77], v[182:185], v[206:209], v[74:77]
	v_mfma_f32_16x16x32_bf16 v[70:73], v[174:177], v[214:217], v[70:73]
	v_mfma_f32_16x16x32_bf16 v[66:69], v[182:185], v[214:217], v[66:69]
	s_barrier
	s_setprio 0
	s_add_i32 s30, s60, s38
	v_lshl_add_u64 v[146:147], v[146:147], 0, s[10:11]
	s_mov_b32 m0, s30
	ds_read_b128 v[186:189], v152 offset:49152
	ds_read_b128 v[190:193], v152 offset:50176
	ds_read_b128 v[194:197], v152 offset:51200
	ds_read_b128 v[198:201], v152 offset:52224
	ds_read_b128 v[202:205], v152 offset:53248
	ds_read_b128 v[206:209], v152 offset:54272
	ds_read_b128 v[210:213], v152 offset:55296
	ds_read_b128 v[214:217], v152 offset:56320
	global_load_lds_dwordx4 v[146:147], off
	s_add_i32 m0, s30, 0x2000
	s_add_u32 s28, s28, 0x160080
	v_lshl_add_u64 v[146:147], v[218:219], 0, s[10:11]
	s_addc_u32 s29, s29, 0
	s_add_i32 s30, s61, s38
	global_load_lds_dwordx4 v[146:147], off
	v_lshl_add_u64 v[146:147], s[28:29], 0, v[132:133]
	s_mov_b32 m0, s30
	s_nop 0
	global_load_lds_dwordx4 v[146:147], off
	v_lshl_add_u64 v[146:147], s[28:29], 0, v[136:137]
	s_add_i32 m0, s30, 0x2000
	s_nop 0
	global_load_lds_dwordx4 v[146:147], off
	v_lshl_add_u64 v[146:147], v[220:221], 0, s[10:11]
	s_mov_b32 m0, s44
	s_nop 0
	global_load_lds_dwordx4 v[146:147], off
	v_lshl_add_u64 v[146:147], v[222:223], 0, s[10:11]
	s_mov_b32 m0, s45
	s_nop 0
	global_load_lds_dwordx4 v[146:147], off
	s_waitcnt vmcnt(8)
	s_waitcnt lgkmcnt(0)
	s_setprio 1
	s_barrier
	v_mfma_f32_16x16x32_bf16 v[62:65], v[154:157], v[186:189], v[62:65]
	v_mfma_f32_16x16x32_bf16 v[58:61], v[162:165], v[186:189], v[58:61]
	v_mfma_f32_16x16x32_bf16 v[54:57], v[154:157], v[194:197], v[54:57]
	v_mfma_f32_16x16x32_bf16 v[46:49], v[162:165], v[194:197], v[46:49]
	v_mfma_f32_16x16x32_bf16 v[38:41], v[154:157], v[202:205], v[38:41]
	v_mfma_f32_16x16x32_bf16 v[30:33], v[162:165], v[202:205], v[30:33]
	v_mfma_f32_16x16x32_bf16 v[22:25], v[154:157], v[210:213], v[22:25]
	v_mfma_f32_16x16x32_bf16 v[14:17], v[162:165], v[210:213], v[14:17]
	v_mfma_f32_16x16x32_bf16 v[62:65], v[158:161], v[190:193], v[62:65]
	v_mfma_f32_16x16x32_bf16 v[58:61], v[166:169], v[190:193], v[58:61]
	v_mfma_f32_16x16x32_bf16 v[54:57], v[158:161], v[198:201], v[54:57]
	v_mfma_f32_16x16x32_bf16 v[46:49], v[166:169], v[198:201], v[46:49]
	v_mfma_f32_16x16x32_bf16 v[38:41], v[158:161], v[206:209], v[38:41]
	v_mfma_f32_16x16x32_bf16 v[30:33], v[166:169], v[206:209], v[30:33]
	v_mfma_f32_16x16x32_bf16 v[22:25], v[158:161], v[214:217], v[22:25]
	v_mfma_f32_16x16x32_bf16 v[14:17], v[166:169], v[214:217], v[14:17]
	s_setprio 0
	s_setprio 1
	v_mfma_f32_16x16x32_bf16 v[50:53], v[170:173], v[186:189], v[50:53]
	v_mfma_f32_16x16x32_bf16 v[42:45], v[178:181], v[186:189], v[42:45]
	v_mfma_f32_16x16x32_bf16 v[34:37], v[170:173], v[194:197], v[34:37]
	v_mfma_f32_16x16x32_bf16 v[26:29], v[178:181], v[194:197], v[26:29]
	v_mfma_f32_16x16x32_bf16 v[18:21], v[170:173], v[202:205], v[18:21]
	v_mfma_f32_16x16x32_bf16 v[10:13], v[178:181], v[202:205], v[10:13]
	v_mfma_f32_16x16x32_bf16 v[6:9], v[170:173], v[210:213], v[6:9]
	v_mfma_f32_16x16x32_bf16 v[2:5], v[178:181], v[210:213], v[2:5]
	v_mfma_f32_16x16x32_bf16 v[50:53], v[174:177], v[190:193], v[50:53]
	v_mfma_f32_16x16x32_bf16 v[42:45], v[182:185], v[190:193], v[42:45]
	v_mfma_f32_16x16x32_bf16 v[34:37], v[174:177], v[198:201], v[34:37]
	v_mfma_f32_16x16x32_bf16 v[26:29], v[182:185], v[198:201], v[26:29]
	v_mfma_f32_16x16x32_bf16 v[18:21], v[174:177], v[206:209], v[18:21]
	v_mfma_f32_16x16x32_bf16 v[10:13], v[182:185], v[206:209], v[10:13]
	v_mfma_f32_16x16x32_bf16 v[6:9], v[174:177], v[214:217], v[6:9]
	v_mfma_f32_16x16x32_bf16 v[2:5], v[182:185], v[214:217], v[2:5]
	s_barrier
	s_setprio 0
	s_add_i32 s59, s59, 2
	s_add_u32 s26, s26, 0x100
	s_addc_u32 s27, s27, 0
	s_add_u32 s57, s57, 0x100
	s_addc_u32 s58, s58, 0
	s_cmpk_gt_u32 s59, 0x55

.LBB0_1696:
	s_ashr_i32 s37, s36, 31
	s_lshl_b64 s[38:39], s[36:37], 20
	s_add_u32 s38, s20, s38
	s_addc_u32 s39, s21, s39
	s_and_b64 s[40:41], s[10:11], exec
	s_cselect_b32 s37, s39, s47
	s_cselect_b32 s43, s38, s46
	s_ashr_i32 s35, s34, 31
	s_lshl_b64 s[40:41], s[34:35], 20
	s_add_u32 s40, s23, s40
	s_addc_u32 s41, s33, s41
	s_and_b64 s[50:51], s[10:11], exec
	s_cselect_b32 s35, s41, s49
	s_cselect_b32 s45, s40, s48
	s_add_u32 s46, s46, 0x80080
	s_addc_u32 s47, s47, 0
	s_add_u32 s69, s48, 0x100
	s_addc_u32 s70, s49, 0
	s_mov_b32 s71, -2
	s_waitcnt vmcnt(0)
	ds_read_b128 v[156:159], v176
	ds_read_b128 v[160:163], v176 offset:1024
	ds_read_b128 v[164:167], v176 offset:2048
	ds_read_b128 v[168:171], v176 offset:3072
	ds_read_b128 v[180:183], v177
	ds_read_b128 v[184:187], v177 offset:1024
	ds_read_b128 v[188:191], v177 offset:2048
	ds_read_b128 v[192:195], v177 offset:3072
	s_add_u32 s48, s46, 0xfff80080
	s_addc_u32 s49, s47, -1
	s_cmp_eq_u32 s71, 28
	s_cselect_b32 s51, s37, s49
	s_cselect_b32 s50, s43, s48
	s_cselect_b32 s49, s35, s70
	s_cselect_b32 s48, s45, s69
	v_lshl_add_u64 v[172:173], s[46:47], 0, v[148:149]
	s_add_i32 m0, s53, 0xc000
	ds_read_b128 v[196:199], v178
	ds_read_b128 v[200:203], v178 offset:1024
	ds_read_b128 v[204:207], v178 offset:2048
	ds_read_b128 v[208:211], v178 offset:3072
	ds_read_b128 v[212:215], v178 offset:4096
	ds_read_b128 v[216:219], v178 offset:5120
	ds_read_b128 v[220:223], v178 offset:6144
	ds_read_b128 v[224:227], v178 offset:7168
	global_load_lds_dwordx4 v[172:173], off
	v_lshl_add_u64 v[172:173], s[46:47], 0, v[150:151]
	s_add_i32 m0, s53, 0xe000
	s_nop 0
	global_load_lds_dwordx4 v[172:173], off
	s_waitcnt vmcnt(8)
	s_waitcnt lgkmcnt(0)
	s_setprio 1
	s_barrier
	v_mfma_f32_16x16x32_bf16 v[126:129], v[156:159], v[196:199], 0
	v_mfma_f32_16x16x32_bf16 v[122:125], v[164:167], v[196:199], 0
	v_mfma_f32_16x16x32_bf16 v[118:121], v[156:159], v[204:207], 0
	v_mfma_f32_16x16x32_bf16 v[114:117], v[164:167], v[204:207], 0
	v_mfma_f32_16x16x32_bf16 v[110:113], v[156:159], v[212:215], 0
	v_mfma_f32_16x16x32_bf16 v[106:109], v[164:167], v[212:215], 0
	v_mfma_f32_16x16x32_bf16 v[102:105], v[156:159], v[220:223], 0
	v_mfma_f32_16x16x32_bf16 v[98:101], v[164:167], v[220:223], 0
	v_mfma_f32_16x16x32_bf16 v[126:129], v[160:163], v[200:203], v[126:129]
	v_mfma_f32_16x16x32_bf16 v[122:125], v[168:171], v[200:203], v[122:125]
	v_mfma_f32_16x16x32_bf16 v[118:121], v[160:163], v[208:211], v[118:121]
	v_mfma_f32_16x16x32_bf16 v[114:117], v[168:171], v[208:211], v[114:117]
	v_mfma_f32_16x16x32_bf16 v[110:113], v[160:163], v[216:219], v[110:113]
	v_mfma_f32_16x16x32_bf16 v[106:109], v[168:171], v[216:219], v[106:109]
	v_mfma_f32_16x16x32_bf16 v[102:105], v[160:163], v[224:227], v[102:105]
	v_mfma_f32_16x16x32_bf16 v[98:101], v[168:171], v[224:227], v[98:101]
	s_setprio 0
	s_setprio 1
	v_mfma_f32_16x16x32_bf16 v[38:41], v[180:183], v[196:199], 0
	v_mfma_f32_16x16x32_bf16 v[34:37], v[188:191], v[196:199], 0
	v_mfma_f32_16x16x32_bf16 v[46:49], v[180:183], v[204:207], 0
	v_mfma_f32_16x16x32_bf16 v[42:45], v[188:191], v[204:207], 0
	v_mfma_f32_16x16x32_bf16 v[54:57], v[180:183], v[212:215], 0
	v_mfma_f32_16x16x32_bf16 v[50:53], v[188:191], v[212:215], 0
	v_mfma_f32_16x16x32_bf16 v[62:65], v[180:183], v[220:223], 0
	v_mfma_f32_16x16x32_bf16 v[58:61], v[188:191], v[220:223], 0
	v_mfma_f32_16x16x32_bf16 v[38:41], v[184:187], v[200:203], v[38:41]
	v_mfma_f32_16x16x32_bf16 v[34:37], v[192:195], v[200:203], v[34:37]
	v_mfma_f32_16x16x32_bf16 v[46:49], v[184:187], v[208:211], v[46:49]
	v_mfma_f32_16x16x32_bf16 v[42:45], v[192:195], v[208:211], v[42:45]
	v_mfma_f32_16x16x32_bf16 v[54:57], v[184:187], v[216:219], v[54:57]
	v_mfma_f32_16x16x32_bf16 v[50:53], v[192:195], v[216:219], v[50:53]
	v_mfma_f32_16x16x32_bf16 v[62:65], v[184:187], v[224:227], v[62:65]
	v_mfma_f32_16x16x32_bf16 v[58:61], v[192:195], v[224:227], v[58:61]
	s_barrier
	s_setprio 0
	s_add_i32 s72, s65, s52
	v_lshl_add_u64 v[172:173], s[48:49], 0, v[132:133]
	s_mov_b32 m0, s72
	ds_read_b128 v[196:199], v178 offset:16384
	ds_read_b128 v[200:203], v178 offset:17408
	ds_read_b128 v[204:207], v178 offset:18432
	ds_read_b128 v[208:211], v178 offset:19456
	ds_read_b128 v[212:215], v178 offset:20480
	ds_read_b128 v[216:219], v178 offset:21504
	ds_read_b128 v[220:223], v178 offset:22528
	ds_read_b128 v[224:227], v178 offset:23552
	global_load_lds_dwordx4 v[172:173], off
	s_add_i32 m0, s72, 0x2000
	s_add_u32 s72, s48, 0x80000
	v_lshl_add_u64 v[228:229], s[48:49], 0, v[136:137]
	s_addc_u32 s73, s49, 0
	s_add_i32 s74, s66, s52
	global_load_lds_dwordx4 v[228:229], off
	v_lshl_add_u64 v[230:231], s[72:73], 0, v[132:133]
	s_mov_b32 m0, s74
	v_lshl_add_u64 v[232:233], s[50:51], 0, v[134:135]
	global_load_lds_dwordx4 v[230:231], off
	v_lshl_add_u64 v[230:231], s[72:73], 0, v[136:137]
	s_add_i32 m0, s74, 0x2000
	s_nop 0
	global_load_lds_dwordx4 v[230:231], off
	v_lshl_add_u64 v[230:231], s[50:51], 0, v[130:131]
	s_mov_b32 m0, s53
	s_nop 0
	global_load_lds_dwordx4 v[230:231], off
	s_mov_b32 m0, s54
	s_nop 0
	global_load_lds_dwordx4 v[232:233], off
	s_waitcnt vmcnt(8)
	s_waitcnt lgkmcnt(0)
	s_setprio 1
	s_barrier
	v_mfma_f32_16x16x32_bf16 v[94:97], v[156:159], v[196:199], 0
	v_mfma_f32_16x16x32_bf16 v[90:93], v[164:167], v[196:199], 0
	v_mfma_f32_16x16x32_bf16 v[86:89], v[156:159], v[204:207], 0
	v_mfma_f32_16x16x32_bf16 v[82:85], v[164:167], v[204:207], 0
	v_mfma_f32_16x16x32_bf16 v[78:81], v[156:159], v[212:215], 0
	v_mfma_f32_16x16x32_bf16 v[74:77], v[164:167], v[212:215], 0
	v_mfma_f32_16x16x32_bf16 v[70:73], v[156:159], v[220:223], 0
	v_mfma_f32_16x16x32_bf16 v[66:69], v[164:167], v[220:223], 0
	v_mfma_f32_16x16x32_bf16 v[94:97], v[160:163], v[200:203], v[94:97]
	v_mfma_f32_16x16x32_bf16 v[90:93], v[168:171], v[200:203], v[90:93]
	v_mfma_f32_16x16x32_bf16 v[86:89], v[160:163], v[208:211], v[86:89]
	v_mfma_f32_16x16x32_bf16 v[82:85], v[168:171], v[208:211], v[82:85]
	v_mfma_f32_16x16x32_bf16 v[78:81], v[160:163], v[216:219], v[78:81]
	v_mfma_f32_16x16x32_bf16 v[74:77], v[168:171], v[216:219], v[74:77]
	v_mfma_f32_16x16x32_bf16 v[70:73], v[160:163], v[224:227], v[70:73]
	v_mfma_f32_16x16x32_bf16 v[66:69], v[168:171], v[224:227], v[66:69]
	s_setprio 0
	s_setprio 1
	v_mfma_f32_16x16x32_bf16 v[6:9], v[180:183], v[196:199], 0
	v_mfma_f32_16x16x32_bf16 v[2:5], v[188:191], v[196:199], 0
	v_mfma_f32_16x16x32_bf16 v[18:21], v[180:183], v[204:207], 0
	v_mfma_f32_16x16x32_bf16 v[14:17], v[188:191], v[204:207], 0
	v_mfma_f32_16x16x32_bf16 v[26:29], v[180:183], v[212:215], 0
	v_mfma_f32_16x16x32_bf16 v[22:25], v[188:191], v[212:215], 0
	v_mfma_f32_16x16x32_bf16 v[30:33], v[180:183], v[220:223], 0
	v_mfma_f32_16x16x32_bf16 v[10:13], v[188:191], v[220:223], 0
	v_mfma_f32_16x16x32_bf16 v[6:9], v[184:187], v[200:203], v[6:9]
	v_mfma_f32_16x16x32_bf16 v[2:5], v[192:195], v[200:203], v[2:5]
	v_mfma_f32_16x16x32_bf16 v[18:21], v[184:187], v[208:211], v[18:21]
	v_mfma_f32_16x16x32_bf16 v[14:17], v[192:195], v[208:211], v[14:17]
	v_mfma_f32_16x16x32_bf16 v[26:29], v[184:187], v[216:219], v[26:29]
	v_mfma_f32_16x16x32_bf16 v[22:25], v[192:195], v[216:219], v[22:25]
	v_mfma_f32_16x16x32_bf16 v[30:33], v[184:187], v[224:227], v[30:33]
	v_mfma_f32_16x16x32_bf16 v[10:13], v[192:195], v[224:227], v[10:13]
	s_barrier
	s_setprio 0
	s_add_i32 s72, 0, 0x18000
	v_add_u32_e32 v138, s72, v174
	s_add_i32 s73, 0, 0x1c000
	ds_read_b128 v[156:159], v138
	ds_read_b128 v[160:163], v138 offset:1024
	ds_read_b128 v[164:167], v138 offset:2048
	ds_read_b128 v[168:171], v138 offset:3072
	v_add_u32_e32 v138, s73, v174
	ds_read_b128 v[180:183], v138
	ds_read_b128 v[184:187], v138 offset:1024
	ds_read_b128 v[188:191], v138 offset:2048
	ds_read_b128 v[192:195], v138 offset:3072
	s_add_u32 s50, s50, 0x80000
	s_addc_u32 s51, s51, 0
	s_mov_b32 m0, s55
	v_lshl_add_u64 v[234:235], s[50:51], 0, v[130:131]
	ds_read_b128 v[196:199], v178 offset:32768
	ds_read_b128 v[200:203], v178 offset:33792
	ds_read_b128 v[204:207], v178 offset:34816
	ds_read_b128 v[208:211], v178 offset:35840
	ds_read_b128 v[212:215], v178 offset:36864
	ds_read_b128 v[216:219], v178 offset:37888
	ds_read_b128 v[220:223], v178 offset:38912
	ds_read_b128 v[224:227], v178 offset:39936
	global_load_lds_dwordx4 v[234:235], off
	v_lshl_add_u64 v[234:235], s[50:51], 0, v[134:135]
	s_mov_b32 m0, s56
	s_nop 0
	global_load_lds_dwordx4 v[234:235], off
	s_waitcnt vmcnt(8)
	s_waitcnt lgkmcnt(0)
	s_setprio 1
	s_barrier
	v_mfma_f32_16x16x32_bf16 v[126:129], v[156:159], v[196:199], v[126:129]
	v_mfma_f32_16x16x32_bf16 v[122:125], v[164:167], v[196:199], v[122:125]
	v_mfma_f32_16x16x32_bf16 v[118:121], v[156:159], v[204:207], v[118:121]
	v_mfma_f32_16x16x32_bf16 v[114:117], v[164:167], v[204:207], v[114:117]
	v_mfma_f32_16x16x32_bf16 v[110:113], v[156:159], v[212:215], v[110:113]
	v_mfma_f32_16x16x32_bf16 v[106:109], v[164:167], v[212:215], v[106:109]
	v_mfma_f32_16x16x32_bf16 v[102:105], v[156:159], v[220:223], v[102:105]
	v_mfma_f32_16x16x32_bf16 v[98:101], v[164:167], v[220:223], v[98:101]
	v_mfma_f32_16x16x32_bf16 v[126:129], v[160:163], v[200:203], v[126:129]
	v_mfma_f32_16x16x32_bf16 v[122:125], v[168:171], v[200:203], v[122:125]
	v_mfma_f32_16x16x32_bf16 v[118:121], v[160:163], v[208:211], v[118:121]
	v_mfma_f32_16x16x32_bf16 v[114:117], v[168:171], v[208:211], v[114:117]
	v_mfma_f32_16x16x32_bf16 v[110:113], v[160:163], v[216:219], v[110:113]
	v_mfma_f32_16x16x32_bf16 v[106:109], v[168:171], v[216:219], v[106:109]
	v_mfma_f32_16x16x32_bf16 v[102:105], v[160:163], v[224:227], v[102:105]
	v_mfma_f32_16x16x32_bf16 v[98:101], v[168:171], v[224:227], v[98:101]
	s_setprio 0
	s_setprio 1
	v_mfma_f32_16x16x32_bf16 v[38:41], v[180:183], v[196:199], v[38:41]
	v_mfma_f32_16x16x32_bf16 v[34:37], v[188:191], v[196:199], v[34:37]
	v_mfma_f32_16x16x32_bf16 v[46:49], v[180:183], v[204:207], v[46:49]
	v_mfma_f32_16x16x32_bf16 v[42:45], v[188:191], v[204:207], v[42:45]
	v_mfma_f32_16x16x32_bf16 v[54:57], v[180:183], v[212:215], v[54:57]
	v_mfma_f32_16x16x32_bf16 v[50:53], v[188:191], v[212:215], v[50:53]
	v_mfma_f32_16x16x32_bf16 v[62:65], v[180:183], v[220:223], v[62:65]
	v_mfma_f32_16x16x32_bf16 v[58:61], v[188:191], v[220:223], v[58:61]
	v_mfma_f32_16x16x32_bf16 v[38:41], v[184:187], v[200:203], v[38:41]
	v_mfma_f32_16x16x32_bf16 v[34:37], v[192:195], v[200:203], v[34:37]
	v_mfma_f32_16x16x32_bf16 v[46:49], v[184:187], v[208:211], v[46:49]
	v_mfma_f32_16x16x32_bf16 v[42:45], v[192:195], v[208:211], v[42:45]
	v_mfma_f32_16x16x32_bf16 v[54:57], v[184:187], v[216:219], v[54:57]
	v_mfma_f32_16x16x32_bf16 v[50:53], v[192:195], v[216:219], v[50:53]
	v_mfma_f32_16x16x32_bf16 v[62:65], v[184:187], v[224:227], v[62:65]
	v_mfma_f32_16x16x32_bf16 v[58:61], v[192:195], v[224:227], v[58:61]
	s_barrier
	s_setprio 0
	s_add_i32 s50, s72, s52
	v_lshl_add_u64 v[172:173], v[172:173], 0, s[6:7]
	s_mov_b32 m0, s50
	ds_read_b128 v[196:199], v178 offset:49152
	ds_read_b128 v[200:203], v178 offset:50176
	ds_read_b128 v[204:207], v178 offset:51200
	ds_read_b128 v[208:211], v178 offset:52224
	ds_read_b128 v[212:215], v178 offset:53248
	ds_read_b128 v[216:219], v178 offset:54272
	ds_read_b128 v[220:223], v178 offset:55296
	ds_read_b128 v[224:227], v178 offset:56320
	global_load_lds_dwordx4 v[172:173], off
	s_add_i32 m0, s50, 0x2000
	s_add_u32 s48, s48, 0x80080
	v_lshl_add_u64 v[172:173], v[228:229], 0, s[6:7]
	s_addc_u32 s49, s49, 0
	s_add_i32 s50, s73, s52
	global_load_lds_dwordx4 v[172:173], off
	v_lshl_add_u64 v[172:173], s[48:49], 0, v[132:133]
	s_mov_b32 m0, s50
	s_nop 0
	global_load_lds_dwordx4 v[172:173], off
	v_lshl_add_u64 v[172:173], s[48:49], 0, v[136:137]
	s_add_i32 m0, s50, 0x2000
	s_nop 0
	global_load_lds_dwordx4 v[172:173], off
	v_lshl_add_u64 v[172:173], v[230:231], 0, s[6:7]
	s_mov_b32 m0, s61
	s_nop 0
	global_load_lds_dwordx4 v[172:173], off
	v_lshl_add_u64 v[172:173], v[232:233], 0, s[6:7]
	s_mov_b32 m0, s62
	s_nop 0
	global_load_lds_dwordx4 v[172:173], off
	s_waitcnt vmcnt(8)
	s_waitcnt lgkmcnt(0)
	s_setprio 1
	s_barrier
	v_mfma_f32_16x16x32_bf16 v[94:97], v[156:159], v[196:199], v[94:97]
	v_mfma_f32_16x16x32_bf16 v[90:93], v[164:167], v[196:199], v[90:93]
	v_mfma_f32_16x16x32_bf16 v[86:89], v[156:159], v[204:207], v[86:89]
	v_mfma_f32_16x16x32_bf16 v[82:85], v[164:167], v[204:207], v[82:85]
	v_mfma_f32_16x16x32_bf16 v[78:81], v[156:159], v[212:215], v[78:81]
	v_mfma_f32_16x16x32_bf16 v[74:77], v[164:167], v[212:215], v[74:77]
	v_mfma_f32_16x16x32_bf16 v[70:73], v[156:159], v[220:223], v[70:73]
	v_mfma_f32_16x16x32_bf16 v[66:69], v[164:167], v[220:223], v[66:69]
	v_mfma_f32_16x16x32_bf16 v[94:97], v[160:163], v[200:203], v[94:97]
	v_mfma_f32_16x16x32_bf16 v[90:93], v[168:171], v[200:203], v[90:93]
	v_mfma_f32_16x16x32_bf16 v[86:89], v[160:163], v[208:211], v[86:89]
	v_mfma_f32_16x16x32_bf16 v[82:85], v[168:171], v[208:211], v[82:85]
	v_mfma_f32_16x16x32_bf16 v[78:81], v[160:163], v[216:219], v[78:81]
	v_mfma_f32_16x16x32_bf16 v[74:77], v[168:171], v[216:219], v[74:77]
	v_mfma_f32_16x16x32_bf16 v[70:73], v[160:163], v[224:227], v[70:73]
	v_mfma_f32_16x16x32_bf16 v[66:69], v[168:171], v[224:227], v[66:69]
	s_setprio 0
	s_setprio 1
	v_mfma_f32_16x16x32_bf16 v[6:9], v[180:183], v[196:199], v[6:9]
	v_mfma_f32_16x16x32_bf16 v[2:5], v[188:191], v[196:199], v[2:5]
	v_mfma_f32_16x16x32_bf16 v[18:21], v[180:183], v[204:207], v[18:21]
	v_mfma_f32_16x16x32_bf16 v[14:17], v[188:191], v[204:207], v[14:17]
	v_mfma_f32_16x16x32_bf16 v[26:29], v[180:183], v[212:215], v[26:29]
	v_mfma_f32_16x16x32_bf16 v[22:25], v[188:191], v[212:215], v[22:25]
	v_mfma_f32_16x16x32_bf16 v[30:33], v[180:183], v[220:223], v[30:33]
	v_mfma_f32_16x16x32_bf16 v[10:13], v[188:191], v[220:223], v[10:13]
	v_mfma_f32_16x16x32_bf16 v[6:9], v[184:187], v[200:203], v[6:9]
	v_mfma_f32_16x16x32_bf16 v[2:5], v[192:195], v[200:203], v[2:5]
	v_mfma_f32_16x16x32_bf16 v[18:21], v[184:187], v[208:211], v[18:21]
	v_mfma_f32_16x16x32_bf16 v[14:17], v[192:195], v[208:211], v[14:17]
	v_mfma_f32_16x16x32_bf16 v[26:29], v[184:187], v[216:219], v[26:29]
	v_mfma_f32_16x16x32_bf16 v[22:25], v[192:195], v[216:219], v[22:25]
	v_mfma_f32_16x16x32_bf16 v[30:33], v[184:187], v[224:227], v[30:33]
	v_mfma_f32_16x16x32_bf16 v[10:13], v[192:195], v[224:227], v[10:13]
	s_barrier
	s_setprio 0
	s_add_i32 s71, s71, 2
	s_add_u32 s46, s46, 0x100
	s_addc_u32 s47, s47, 0
	s_add_u32 s69, s69, 0x100
	s_addc_u32 s70, s70, 0
	s_cmp_gt_u32 s71, 29

.LBB0_2113:
	s_ashr_i32 s25, s24, 31
	s_lshl_b64 s[26:27], s[24:25], 20
	v_readlane_b32 s28, v254, 22
	v_readlane_b32 s29, v254, 23
	s_add_u32 s26, s28, s26
	s_addc_u32 s27, s29, s27
	s_and_b64 s[28:29], s[4:5], exec
	s_cselect_b32 s25, s27, s35
	s_cselect_b32 s57, s26, s34
	s_ashr_i32 s23, s22, 31
	s_lshl_b64 s[28:29], s[22:23], 20
	s_add_u32 s28, s40, s28
	s_addc_u32 s29, s41, s29
	s_and_b64 s[38:39], s[4:5], exec
	s_cselect_b32 s23, s29, s37
	s_cselect_b32 s58, s28, s36
	s_add_u32 s34, s34, 0x80080
	s_addc_u32 s35, s35, 0
	s_add_u32 s59, s36, 0x100
	s_addc_u32 s60, s37, 0
	s_mov_b32 s61, -2
	ds_read_b128 v[154:157], v150
	ds_read_b128 v[158:161], v150 offset:1024
	ds_read_b128 v[162:165], v150 offset:2048
	ds_read_b128 v[166:169], v150 offset:3072
	ds_read_b128 v[170:173], v151
	ds_read_b128 v[174:177], v151 offset:1024
	ds_read_b128 v[178:181], v151 offset:2048
	ds_read_b128 v[182:185], v151 offset:3072
	s_add_u32 s36, s34, 0xfff80080
	s_addc_u32 s37, s35, -1
	s_cmp_eq_u32 s61, 28
	s_cselect_b32 s39, s25, s37
	s_cselect_b32 s38, s57, s36
	s_cselect_b32 s37, s23, s60
	s_cselect_b32 s36, s58, s59
	v_lshl_add_u64 v[146:147], s[34:35], 0, v[138:139]
	s_add_i32 m0, s31, 0xc000
	ds_read_b128 v[186:189], v152
	ds_read_b128 v[190:193], v152 offset:1024
	ds_read_b128 v[194:197], v152 offset:2048
	ds_read_b128 v[198:201], v152 offset:3072
	ds_read_b128 v[202:205], v152 offset:4096
	ds_read_b128 v[206:209], v152 offset:5120
	ds_read_b128 v[210:213], v152 offset:6144
	ds_read_b128 v[214:217], v152 offset:7168
	global_load_lds_dwordx4 v[146:147], off
	v_lshl_add_u64 v[146:147], s[34:35], 0, v[140:141]
	s_add_i32 m0, s31, 0xe000
	s_nop 0
	global_load_lds_dwordx4 v[146:147], off
	s_waitcnt vmcnt(8)
	s_waitcnt lgkmcnt(0)
	s_setprio 1
	s_barrier
	v_mfma_f32_16x16x32_bf16 v[126:129], v[154:157], v[186:189], 0
	v_mfma_f32_16x16x32_bf16 v[122:125], v[162:165], v[186:189], 0
	v_mfma_f32_16x16x32_bf16 v[118:121], v[154:157], v[194:197], 0
	v_mfma_f32_16x16x32_bf16 v[110:113], v[162:165], v[194:197], 0
	v_mfma_f32_16x16x32_bf16 v[102:105], v[154:157], v[202:205], 0
	v_mfma_f32_16x16x32_bf16 v[94:97], v[162:165], v[202:205], 0
	v_mfma_f32_16x16x32_bf16 v[86:89], v[154:157], v[210:213], 0
	v_mfma_f32_16x16x32_bf16 v[78:81], v[162:165], v[210:213], 0
	v_mfma_f32_16x16x32_bf16 v[126:129], v[158:161], v[190:193], v[126:129]
	v_mfma_f32_16x16x32_bf16 v[122:125], v[166:169], v[190:193], v[122:125]
	v_mfma_f32_16x16x32_bf16 v[118:121], v[158:161], v[198:201], v[118:121]
	v_mfma_f32_16x16x32_bf16 v[110:113], v[166:169], v[198:201], v[110:113]
	v_mfma_f32_16x16x32_bf16 v[102:105], v[158:161], v[206:209], v[102:105]
	v_mfma_f32_16x16x32_bf16 v[94:97], v[166:169], v[206:209], v[94:97]
	v_mfma_f32_16x16x32_bf16 v[86:89], v[158:161], v[214:217], v[86:89]
	v_mfma_f32_16x16x32_bf16 v[78:81], v[166:169], v[214:217], v[78:81]
	s_setprio 0
	s_setprio 1
	v_mfma_f32_16x16x32_bf16 v[114:117], v[170:173], v[186:189], 0
	v_mfma_f32_16x16x32_bf16 v[106:109], v[178:181], v[186:189], 0
	v_mfma_f32_16x16x32_bf16 v[98:101], v[170:173], v[194:197], 0
	v_mfma_f32_16x16x32_bf16 v[90:93], v[178:181], v[194:197], 0
	v_mfma_f32_16x16x32_bf16 v[82:85], v[170:173], v[202:205], 0
	v_mfma_f32_16x16x32_bf16 v[74:77], v[178:181], v[202:205], 0
	v_mfma_f32_16x16x32_bf16 v[70:73], v[170:173], v[210:213], 0
	v_mfma_f32_16x16x32_bf16 v[66:69], v[178:181], v[210:213], 0
	v_mfma_f32_16x16x32_bf16 v[114:117], v[174:177], v[190:193], v[114:117]
	v_mfma_f32_16x16x32_bf16 v[106:109], v[182:185], v[190:193], v[106:109]
	v_mfma_f32_16x16x32_bf16 v[98:101], v[174:177], v[198:201], v[98:101]
	v_mfma_f32_16x16x32_bf16 v[90:93], v[182:185], v[198:201], v[90:93]
	v_mfma_f32_16x16x32_bf16 v[82:85], v[174:177], v[206:209], v[82:85]
	v_mfma_f32_16x16x32_bf16 v[74:77], v[182:185], v[206:209], v[74:77]
	v_mfma_f32_16x16x32_bf16 v[70:73], v[174:177], v[214:217], v[70:73]
	v_mfma_f32_16x16x32_bf16 v[66:69], v[182:185], v[214:217], v[66:69]
	s_barrier
	s_setprio 0
	s_add_i32 s62, s50, s42
	v_lshl_add_u64 v[146:147], s[36:37], 0, v[132:133]
	s_mov_b32 m0, s62
	ds_read_b128 v[186:189], v152 offset:16384
	ds_read_b128 v[190:193], v152 offset:17408
	ds_read_b128 v[194:197], v152 offset:18432
	ds_read_b128 v[198:201], v152 offset:19456
	ds_read_b128 v[202:205], v152 offset:20480
	ds_read_b128 v[206:209], v152 offset:21504
	ds_read_b128 v[210:213], v152 offset:22528
	ds_read_b128 v[214:217], v152 offset:23552
	global_load_lds_dwordx4 v[146:147], off
	s_add_i32 m0, s62, 0x2000
	s_add_u32 s62, s36, 0x80000
	v_lshl_add_u64 v[218:219], s[36:37], 0, v[136:137]
	s_addc_u32 s63, s37, 0
	s_add_i32 s64, s51, s42
	global_load_lds_dwordx4 v[218:219], off
	v_lshl_add_u64 v[220:221], s[62:63], 0, v[132:133]
	s_mov_b32 m0, s64
	v_lshl_add_u64 v[222:223], s[38:39], 0, v[134:135]
	global_load_lds_dwordx4 v[220:221], off
	v_lshl_add_u64 v[220:221], s[62:63], 0, v[136:137]
	s_add_i32 m0, s64, 0x2000
	s_nop 0
	global_load_lds_dwordx4 v[220:221], off
	v_lshl_add_u64 v[220:221], s[38:39], 0, v[130:131]
	s_mov_b32 m0, s31
	s_nop 0
	global_load_lds_dwordx4 v[220:221], off
	s_mov_b32 m0, s43
	s_nop 0
	global_load_lds_dwordx4 v[222:223], off
	s_waitcnt vmcnt(8)
	s_waitcnt lgkmcnt(0)
	s_setprio 1
	s_barrier
	v_mfma_f32_16x16x32_bf16 v[62:65], v[154:157], v[186:189], 0
	v_mfma_f32_16x16x32_bf16 v[58:61], v[162:165], v[186:189], 0
	v_mfma_f32_16x16x32_bf16 v[54:57], v[154:157], v[194:197], 0
	v_mfma_f32_16x16x32_bf16 v[46:49], v[162:165], v[194:197], 0
	v_mfma_f32_16x16x32_bf16 v[38:41], v[154:157], v[202:205], 0
	v_mfma_f32_16x16x32_bf16 v[30:33], v[162:165], v[202:205], 0
	v_mfma_f32_16x16x32_bf16 v[22:25], v[154:157], v[210:213], 0
	v_mfma_f32_16x16x32_bf16 v[14:17], v[162:165], v[210:213], 0
	v_mfma_f32_16x16x32_bf16 v[62:65], v[158:161], v[190:193], v[62:65]
	v_mfma_f32_16x16x32_bf16 v[58:61], v[166:169], v[190:193], v[58:61]
	v_mfma_f32_16x16x32_bf16 v[54:57], v[158:161], v[198:201], v[54:57]
	v_mfma_f32_16x16x32_bf16 v[46:49], v[166:169], v[198:201], v[46:49]
	v_mfma_f32_16x16x32_bf16 v[38:41], v[158:161], v[206:209], v[38:41]
	v_mfma_f32_16x16x32_bf16 v[30:33], v[166:169], v[206:209], v[30:33]
	v_mfma_f32_16x16x32_bf16 v[22:25], v[158:161], v[214:217], v[22:25]
	v_mfma_f32_16x16x32_bf16 v[14:17], v[166:169], v[214:217], v[14:17]
	s_setprio 0
	s_setprio 1
	v_mfma_f32_16x16x32_bf16 v[50:53], v[170:173], v[186:189], 0
	v_mfma_f32_16x16x32_bf16 v[42:45], v[178:181], v[186:189], 0
	v_mfma_f32_16x16x32_bf16 v[34:37], v[170:173], v[194:197], 0
	v_mfma_f32_16x16x32_bf16 v[26:29], v[178:181], v[194:197], 0
	v_mfma_f32_16x16x32_bf16 v[18:21], v[170:173], v[202:205], 0
	v_mfma_f32_16x16x32_bf16 v[10:13], v[178:181], v[202:205], 0
	v_mfma_f32_16x16x32_bf16 v[6:9], v[170:173], v[210:213], 0
	v_mfma_f32_16x16x32_bf16 v[2:5], v[178:181], v[210:213], 0
	v_mfma_f32_16x16x32_bf16 v[50:53], v[174:177], v[190:193], v[50:53]
	v_mfma_f32_16x16x32_bf16 v[42:45], v[182:185], v[190:193], v[42:45]
	v_mfma_f32_16x16x32_bf16 v[34:37], v[174:177], v[198:201], v[34:37]
	v_mfma_f32_16x16x32_bf16 v[26:29], v[182:185], v[198:201], v[26:29]
	v_mfma_f32_16x16x32_bf16 v[18:21], v[174:177], v[206:209], v[18:21]
	v_mfma_f32_16x16x32_bf16 v[10:13], v[182:185], v[206:209], v[10:13]
	v_mfma_f32_16x16x32_bf16 v[6:9], v[174:177], v[214:217], v[6:9]
	v_mfma_f32_16x16x32_bf16 v[2:5], v[182:185], v[214:217], v[2:5]
	s_barrier
	s_setprio 0
	s_add_i32 s62, 0, 0x18000
	v_add_u32_e32 v153, s62, v148
	s_add_i32 s63, 0, 0x1c000
	ds_read_b128 v[154:157], v153
	ds_read_b128 v[158:161], v153 offset:1024
	ds_read_b128 v[162:165], v153 offset:2048
	ds_read_b128 v[166:169], v153 offset:3072
	v_add_u32_e32 v153, s63, v148
	ds_read_b128 v[170:173], v153
	ds_read_b128 v[174:177], v153 offset:1024
	ds_read_b128 v[178:181], v153 offset:2048
	ds_read_b128 v[182:185], v153 offset:3072
	s_add_u32 s38, s38, 0x80000
	s_addc_u32 s39, s39, 0
	s_mov_b32 m0, s44
	v_lshl_add_u64 v[224:225], s[38:39], 0, v[130:131]
	ds_read_b128 v[186:189], v152 offset:32768
	ds_read_b128 v[190:193], v152 offset:33792
	ds_read_b128 v[194:197], v152 offset:34816
	ds_read_b128 v[198:201], v152 offset:35840
	ds_read_b128 v[202:205], v152 offset:36864
	ds_read_b128 v[206:209], v152 offset:37888
	ds_read_b128 v[210:213], v152 offset:38912
	ds_read_b128 v[214:217], v152 offset:39936
	global_load_lds_dwordx4 v[224:225], off
	v_lshl_add_u64 v[224:225], s[38:39], 0, v[134:135]
	s_mov_b32 m0, s45
	s_nop 0
	global_load_lds_dwordx4 v[224:225], off
	s_waitcnt vmcnt(8)
	s_waitcnt lgkmcnt(0)
	s_setprio 1
	s_barrier
	v_mfma_f32_16x16x32_bf16 v[126:129], v[154:157], v[186:189], v[126:129]
	v_mfma_f32_16x16x32_bf16 v[122:125], v[162:165], v[186:189], v[122:125]
	v_mfma_f32_16x16x32_bf16 v[118:121], v[154:157], v[194:197], v[118:121]
	v_mfma_f32_16x16x32_bf16 v[110:113], v[162:165], v[194:197], v[110:113]
	v_mfma_f32_16x16x32_bf16 v[102:105], v[154:157], v[202:205], v[102:105]
	v_mfma_f32_16x16x32_bf16 v[94:97], v[162:165], v[202:205], v[94:97]
	v_mfma_f32_16x16x32_bf16 v[86:89], v[154:157], v[210:213], v[86:89]
	v_mfma_f32_16x16x32_bf16 v[78:81], v[162:165], v[210:213], v[78:81]
	v_mfma_f32_16x16x32_bf16 v[126:129], v[158:161], v[190:193], v[126:129]
	v_mfma_f32_16x16x32_bf16 v[122:125], v[166:169], v[190:193], v[122:125]
	v_mfma_f32_16x16x32_bf16 v[118:121], v[158:161], v[198:201], v[118:121]
	v_mfma_f32_16x16x32_bf16 v[110:113], v[166:169], v[198:201], v[110:113]
	v_mfma_f32_16x16x32_bf16 v[102:105], v[158:161], v[206:209], v[102:105]
	v_mfma_f32_16x16x32_bf16 v[94:97], v[166:169], v[206:209], v[94:97]
	v_mfma_f32_16x16x32_bf16 v[86:89], v[158:161], v[214:217], v[86:89]
	v_mfma_f32_16x16x32_bf16 v[78:81], v[166:169], v[214:217], v[78:81]
	s_setprio 0
	s_setprio 1
	v_mfma_f32_16x16x32_bf16 v[114:117], v[170:173], v[186:189], v[114:117]
	v_mfma_f32_16x16x32_bf16 v[106:109], v[178:181], v[186:189], v[106:109]
	v_mfma_f32_16x16x32_bf16 v[98:101], v[170:173], v[194:197], v[98:101]
	v_mfma_f32_16x16x32_bf16 v[90:93], v[178:181], v[194:197], v[90:93]
	v_mfma_f32_16x16x32_bf16 v[82:85], v[170:173], v[202:205], v[82:85]
	v_mfma_f32_16x16x32_bf16 v[74:77], v[178:181], v[202:205], v[74:77]
	v_mfma_f32_16x16x32_bf16 v[70:73], v[170:173], v[210:213], v[70:73]
	v_mfma_f32_16x16x32_bf16 v[66:69], v[178:181], v[210:213], v[66:69]
	v_mfma_f32_16x16x32_bf16 v[114:117], v[174:177], v[190:193], v[114:117]
	v_mfma_f32_16x16x32_bf16 v[106:109], v[182:185], v[190:193], v[106:109]
	v_mfma_f32_16x16x32_bf16 v[98:101], v[174:177], v[198:201], v[98:101]
	v_mfma_f32_16x16x32_bf16 v[90:93], v[182:185], v[198:201], v[90:93]
	v_mfma_f32_16x16x32_bf16 v[82:85], v[174:177], v[206:209], v[82:85]
	v_mfma_f32_16x16x32_bf16 v[74:77], v[182:185], v[206:209], v[74:77]
	v_mfma_f32_16x16x32_bf16 v[70:73], v[174:177], v[214:217], v[70:73]
	v_mfma_f32_16x16x32_bf16 v[66:69], v[182:185], v[214:217], v[66:69]
	s_barrier
	s_setprio 0
	s_add_i32 s38, s62, s42
	v_lshl_add_u64 v[146:147], v[146:147], 0, s[10:11]
	s_mov_b32 m0, s38
	ds_read_b128 v[186:189], v152 offset:49152
	ds_read_b128 v[190:193], v152 offset:50176
	ds_read_b128 v[194:197], v152 offset:51200
	ds_read_b128 v[198:201], v152 offset:52224
	ds_read_b128 v[202:205], v152 offset:53248
	ds_read_b128 v[206:209], v152 offset:54272
	ds_read_b128 v[210:213], v152 offset:55296
	ds_read_b128 v[214:217], v152 offset:56320
	global_load_lds_dwordx4 v[146:147], off
	s_add_i32 m0, s38, 0x2000
	s_add_u32 s36, s36, 0x80080
	v_lshl_add_u64 v[146:147], v[218:219], 0, s[10:11]
	s_addc_u32 s37, s37, 0
	s_add_i32 s38, s63, s42
	global_load_lds_dwordx4 v[146:147], off
	v_lshl_add_u64 v[146:147], s[36:37], 0, v[132:133]
	s_mov_b32 m0, s38
	s_nop 0
	global_load_lds_dwordx4 v[146:147], off
	v_lshl_add_u64 v[146:147], s[36:37], 0, v[136:137]
	s_add_i32 m0, s38, 0x2000
	s_nop 0
	global_load_lds_dwordx4 v[146:147], off
	v_lshl_add_u64 v[146:147], v[220:221], 0, s[10:11]
	s_mov_b32 m0, s47
	s_nop 0
	global_load_lds_dwordx4 v[146:147], off
	v_lshl_add_u64 v[146:147], v[222:223], 0, s[10:11]
	s_mov_b32 m0, s48
	s_nop 0
	global_load_lds_dwordx4 v[146:147], off
	s_waitcnt vmcnt(8)
	s_waitcnt lgkmcnt(0)
	s_setprio 1
	s_barrier
	v_mfma_f32_16x16x32_bf16 v[62:65], v[154:157], v[186:189], v[62:65]
	v_mfma_f32_16x16x32_bf16 v[58:61], v[162:165], v[186:189], v[58:61]
	v_mfma_f32_16x16x32_bf16 v[54:57], v[154:157], v[194:197], v[54:57]
	v_mfma_f32_16x16x32_bf16 v[46:49], v[162:165], v[194:197], v[46:49]
	v_mfma_f32_16x16x32_bf16 v[38:41], v[154:157], v[202:205], v[38:41]
	v_mfma_f32_16x16x32_bf16 v[30:33], v[162:165], v[202:205], v[30:33]
	v_mfma_f32_16x16x32_bf16 v[22:25], v[154:157], v[210:213], v[22:25]
	v_mfma_f32_16x16x32_bf16 v[14:17], v[162:165], v[210:213], v[14:17]
	v_mfma_f32_16x16x32_bf16 v[62:65], v[158:161], v[190:193], v[62:65]
	v_mfma_f32_16x16x32_bf16 v[58:61], v[166:169], v[190:193], v[58:61]
	v_mfma_f32_16x16x32_bf16 v[54:57], v[158:161], v[198:201], v[54:57]
	v_mfma_f32_16x16x32_bf16 v[46:49], v[166:169], v[198:201], v[46:49]
	v_mfma_f32_16x16x32_bf16 v[38:41], v[158:161], v[206:209], v[38:41]
	v_mfma_f32_16x16x32_bf16 v[30:33], v[166:169], v[206:209], v[30:33]
	v_mfma_f32_16x16x32_bf16 v[22:25], v[158:161], v[214:217], v[22:25]
	v_mfma_f32_16x16x32_bf16 v[14:17], v[166:169], v[214:217], v[14:17]
	s_setprio 0
	s_setprio 1
	v_mfma_f32_16x16x32_bf16 v[50:53], v[170:173], v[186:189], v[50:53]
	v_mfma_f32_16x16x32_bf16 v[42:45], v[178:181], v[186:189], v[42:45]
	v_mfma_f32_16x16x32_bf16 v[34:37], v[170:173], v[194:197], v[34:37]
	v_mfma_f32_16x16x32_bf16 v[26:29], v[178:181], v[194:197], v[26:29]
	v_mfma_f32_16x16x32_bf16 v[18:21], v[170:173], v[202:205], v[18:21]
	v_mfma_f32_16x16x32_bf16 v[10:13], v[178:181], v[202:205], v[10:13]
	v_mfma_f32_16x16x32_bf16 v[6:9], v[170:173], v[210:213], v[6:9]
	v_mfma_f32_16x16x32_bf16 v[2:5], v[178:181], v[210:213], v[2:5]
	v_mfma_f32_16x16x32_bf16 v[50:53], v[174:177], v[190:193], v[50:53]
	v_mfma_f32_16x16x32_bf16 v[42:45], v[182:185], v[190:193], v[42:45]
	v_mfma_f32_16x16x32_bf16 v[34:37], v[174:177], v[198:201], v[34:37]
	v_mfma_f32_16x16x32_bf16 v[26:29], v[182:185], v[198:201], v[26:29]
	v_mfma_f32_16x16x32_bf16 v[18:21], v[174:177], v[206:209], v[18:21]
	v_mfma_f32_16x16x32_bf16 v[10:13], v[182:185], v[206:209], v[10:13]
	v_mfma_f32_16x16x32_bf16 v[6:9], v[174:177], v[214:217], v[6:9]
	v_mfma_f32_16x16x32_bf16 v[2:5], v[182:185], v[214:217], v[2:5]
	s_barrier
	s_setprio 0
	s_add_i32 s61, s61, 2
	s_add_u32 s34, s34, 0x100
	s_addc_u32 s35, s35, 0
	s_add_u32 s59, s59, 0x100
	s_addc_u32 s60, s60, 0
	s_cmp_gt_u32 s61, 29

.LBB0_2365:
	s_ashr_i32 s23, s22, 31
	s_lshl_b64 s[26:27], s[22:23], 19
	s_add_u32 s26, s19, s26
	s_addc_u32 s27, s40, s27
	s_and_b64 s[28:29], s[4:5], exec
	s_cselect_b32 s23, s27, s35
	s_cselect_b32 s66, s26, s34
	s_ashr_i32 s25, s24, 31
	s_lshl_b64 s[28:29], s[24:25], 19
	s_add_u32 s28, s41, s28
	s_addc_u32 s29, s42, s29
	s_and_b64 s[38:39], s[4:5], exec
	s_cselect_b32 s25, s29, s37
	s_cselect_b32 s67, s28, s36
	s_add_u32 s34, s34, 0x40080
	s_addc_u32 s35, s35, 0
	s_add_u32 s68, s36, 0x100
	s_addc_u32 s69, s37, 0
	s_mov_b32 s70, -2
	ds_read_b128 v[18:21], v186
	ds_read_b128 v[22:25], v186 offset:1024
	ds_read_b128 v[26:29], v186 offset:2048
	ds_read_b128 v[30:33], v186 offset:3072
	ds_read_b128 v[2:5], v187
	ds_read_b128 v[6:9], v187 offset:1024
	ds_read_b128 v[10:13], v187 offset:2048
	ds_read_b128 v[14:17], v187 offset:3072
	s_add_u32 s36, s34, 0xfffc0080
	s_addc_u32 s37, s35, -1
	s_cmp_eq_u32 s70, 12
	s_cselect_b32 s39, s23, s37
	s_cselect_b32 s38, s66, s36
	s_cselect_b32 s37, s25, s69
	s_cselect_b32 s36, s67, s68
	v_lshl_add_u64 v[208:209], s[34:35], 0, v[170:171]
	s_add_i32 m0, s31, 0xc000
	ds_read_b128 v[176:179], v188
	ds_read_b128 v[180:183], v188 offset:1024
	ds_read_b128 v[192:195], v188 offset:2048
	ds_read_b128 v[196:199], v188 offset:3072
	ds_read_b128 v[200:203], v188 offset:4096
	ds_read_b128 v[204:207], v188 offset:5120
	ds_read_b128 v[216:219], v188 offset:6144
	ds_read_b128 v[220:223], v188 offset:7168
	global_load_lds_dwordx4 v[208:209], off
	v_lshl_add_u64 v[208:209], s[34:35], 0, v[172:173]
	s_add_i32 m0, s31, 0xe000
	s_nop 0
	global_load_lds_dwordx4 v[208:209], off
	s_waitcnt vmcnt(8)
	s_waitcnt lgkmcnt(0)
	s_setprio 1
	s_barrier
	v_mfma_scale_f32_16x16x128_f8f6f4 v[158:161], v[18:25], v[176:183], 0, v189, v190 op_sel_hi:[0,0,0]
	v_mfma_scale_f32_16x16x128_f8f6f4 v[150:153], v[26:33], v[176:183], 0, v189, v190 op_sel_hi:[0,0,0]
	v_mfma_scale_f32_16x16x128_f8f6f4 v[142:145], v[18:25], v[192:199], 0, v189, v190 op_sel_hi:[0,0,0]
	v_mfma_scale_f32_16x16x128_f8f6f4 v[134:137], v[26:33], v[192:199], 0, v189, v190 op_sel_hi:[0,0,0]
	v_mfma_scale_f32_16x16x128_f8f6f4 v[126:129], v[18:25], v[200:207], 0, v189, v190 op_sel_hi:[0,0,0]
	v_mfma_scale_f32_16x16x128_f8f6f4 v[118:121], v[26:33], v[200:207], 0, v189, v190 op_sel_hi:[0,0,0]
	v_mfma_scale_f32_16x16x128_f8f6f4 v[110:113], v[18:25], v[216:223], 0, v189, v190 op_sel_hi:[0,0,0]
	v_mfma_scale_f32_16x16x128_f8f6f4 v[102:105], v[26:33], v[216:223], 0, v189, v190 op_sel_hi:[0,0,0]
	s_setprio 0
	s_setprio 1
	v_mfma_scale_f32_16x16x128_f8f6f4 v[154:157], v[2:9], v[176:183], 0, v189, v190 op_sel_hi:[0,0,0]
	v_mfma_scale_f32_16x16x128_f8f6f4 v[146:149], v[10:17], v[176:183], 0, v189, v190 op_sel_hi:[0,0,0]
	v_mfma_scale_f32_16x16x128_f8f6f4 v[138:141], v[2:9], v[192:199], 0, v189, v190 op_sel_hi:[0,0,0]
	v_mfma_scale_f32_16x16x128_f8f6f4 v[130:133], v[10:17], v[192:199], 0, v189, v190 op_sel_hi:[0,0,0]
	v_mfma_scale_f32_16x16x128_f8f6f4 v[122:125], v[2:9], v[200:207], 0, v189, v190 op_sel_hi:[0,0,0]
	v_mfma_scale_f32_16x16x128_f8f6f4 v[114:117], v[10:17], v[200:207], 0, v189, v190 op_sel_hi:[0,0,0]
	v_mfma_scale_f32_16x16x128_f8f6f4 v[106:109], v[2:9], v[216:223], 0, v189, v190 op_sel_hi:[0,0,0]
	v_mfma_scale_f32_16x16x128_f8f6f4 v[98:101], v[10:17], v[216:223], 0, v189, v190 op_sel_hi:[0,0,0]
	s_barrier
	s_setprio 0
	s_add_i32 s71, s60, s43
	v_lshl_add_u64 v[176:177], s[36:37], 0, v[166:167]
	s_mov_b32 m0, s71
	ds_read_b128 v[192:195], v188 offset:16384
	ds_read_b128 v[196:199], v188 offset:17408
	ds_read_b128 v[200:203], v188 offset:18432
	ds_read_b128 v[204:207], v188 offset:19456
	ds_read_b128 v[216:219], v188 offset:20480
	ds_read_b128 v[220:223], v188 offset:21504
	ds_read_b128 v[224:227], v188 offset:22528
	ds_read_b128 v[228:231], v188 offset:23552
	global_load_lds_dwordx4 v[176:177], off
	s_add_i32 m0, s71, 0x2000
	s_add_u32 s72, s36, 0x40000
	v_lshl_add_u64 v[178:179], s[36:37], 0, v[162:163]
	s_addc_u32 s73, s37, 0
	s_add_i32 s71, s61, s43
	global_load_lds_dwordx4 v[178:179], off
	v_lshl_add_u64 v[180:181], s[72:73], 0, v[166:167]
	s_mov_b32 m0, s71
	v_lshl_add_u64 v[182:183], s[38:39], 0, v[164:165]
	global_load_lds_dwordx4 v[180:181], off
	v_lshl_add_u64 v[180:181], s[72:73], 0, v[162:163]
	s_add_i32 m0, s71, 0x2000
	s_nop 0
	global_load_lds_dwordx4 v[180:181], off
	v_lshl_add_u64 v[180:181], s[38:39], 0, v[168:169]
	s_mov_b32 m0, s31
	s_nop 0
	global_load_lds_dwordx4 v[180:181], off
	s_mov_b32 m0, s47
	s_nop 0
	global_load_lds_dwordx4 v[182:183], off
	s_waitcnt vmcnt(8)
	s_waitcnt lgkmcnt(0)
	s_setprio 1
	s_barrier
	v_mfma_scale_f32_16x16x128_f8f6f4 v[94:97], v[18:25], v[192:199], 0, v189, v190 op_sel_hi:[0,0,0]
	v_mfma_scale_f32_16x16x128_f8f6f4 v[86:89], v[26:33], v[192:199], 0, v189, v190 op_sel_hi:[0,0,0]
	v_mfma_scale_f32_16x16x128_f8f6f4 v[78:81], v[18:25], v[200:207], 0, v189, v190 op_sel_hi:[0,0,0]
	v_mfma_scale_f32_16x16x128_f8f6f4 v[70:73], v[26:33], v[200:207], 0, v189, v190 op_sel_hi:[0,0,0]
	v_mfma_scale_f32_16x16x128_f8f6f4 v[62:65], v[18:25], v[216:223], 0, v189, v190 op_sel_hi:[0,0,0]
	v_mfma_scale_f32_16x16x128_f8f6f4 v[54:57], v[26:33], v[216:223], 0, v189, v190 op_sel_hi:[0,0,0]
	v_mfma_scale_f32_16x16x128_f8f6f4 v[46:49], v[18:25], v[224:231], 0, v189, v190 op_sel_hi:[0,0,0]
	v_mfma_scale_f32_16x16x128_f8f6f4 v[38:41], v[26:33], v[224:231], 0, v189, v190 op_sel_hi:[0,0,0]
	s_setprio 0
	s_setprio 1
	v_mfma_scale_f32_16x16x128_f8f6f4 v[90:93], v[2:9], v[192:199], 0, v189, v190 op_sel_hi:[0,0,0]
	v_mfma_scale_f32_16x16x128_f8f6f4 v[82:85], v[10:17], v[192:199], 0, v189, v190 op_sel_hi:[0,0,0]
	v_mfma_scale_f32_16x16x128_f8f6f4 v[74:77], v[2:9], v[200:207], 0, v189, v190 op_sel_hi:[0,0,0]
	v_mfma_scale_f32_16x16x128_f8f6f4 v[66:69], v[10:17], v[200:207], 0, v189, v190 op_sel_hi:[0,0,0]
	v_mfma_scale_f32_16x16x128_f8f6f4 v[58:61], v[2:9], v[216:223], 0, v189, v190 op_sel_hi:[0,0,0]
	v_mfma_scale_f32_16x16x128_f8f6f4 v[50:53], v[10:17], v[216:223], 0, v189, v190 op_sel_hi:[0,0,0]
	v_mfma_scale_f32_16x16x128_f8f6f4 v[42:45], v[2:9], v[224:231], 0, v189, v190 op_sel_hi:[0,0,0]
	v_mfma_scale_f32_16x16x128_f8f6f4 v[34:37], v[10:17], v[224:231], 0, v189, v190 op_sel_hi:[0,0,0]
	s_barrier
	s_setprio 0
	s_add_i32 s71, 0, 0x18000
	s_add_i32 s72, 0, 0x1c000
	v_add_u32_e32 v14, s71, v184
	v_add_u32_e32 v30, s72, v184
	ds_read_b128 v[2:5], v14
	ds_read_b128 v[6:9], v14 offset:1024
	ds_read_b128 v[10:13], v14 offset:2048
	ds_read_b128 v[14:17], v14 offset:3072
	ds_read_b128 v[18:21], v30
	ds_read_b128 v[22:25], v30 offset:1024
	ds_read_b128 v[26:29], v30 offset:2048
	ds_read_b128 v[30:33], v30 offset:3072
	s_add_u32 s38, s38, 0x40000
	s_addc_u32 s39, s39, 0
	s_mov_b32 m0, s48
	v_lshl_add_u64 v[208:209], s[38:39], 0, v[168:169]
	ds_read_b128 v[192:195], v188 offset:32768
	ds_read_b128 v[196:199], v188 offset:33792
	ds_read_b128 v[200:203], v188 offset:34816
	ds_read_b128 v[204:207], v188 offset:35840
	ds_read_b128 v[216:219], v188 offset:36864
	ds_read_b128 v[220:223], v188 offset:37888
	ds_read_b128 v[224:227], v188 offset:38912
	ds_read_b128 v[228:231], v188 offset:39936
	global_load_lds_dwordx4 v[208:209], off
	v_lshl_add_u64 v[208:209], s[38:39], 0, v[164:165]
	s_mov_b32 m0, s49
	s_nop 0
	global_load_lds_dwordx4 v[208:209], off
	s_waitcnt vmcnt(8)
	s_waitcnt lgkmcnt(0)
	s_setprio 1
	s_barrier
	v_mfma_scale_f32_16x16x128_f8f6f4 v[158:161], v[2:9], v[192:199], v[158:161], v189, v190 op_sel_hi:[0,0,0]
	v_mfma_scale_f32_16x16x128_f8f6f4 v[150:153], v[10:17], v[192:199], v[150:153], v189, v190 op_sel_hi:[0,0,0]
	v_mfma_scale_f32_16x16x128_f8f6f4 v[142:145], v[2:9], v[200:207], v[142:145], v189, v190 op_sel_hi:[0,0,0]
	v_mfma_scale_f32_16x16x128_f8f6f4 v[134:137], v[10:17], v[200:207], v[134:137], v189, v190 op_sel_hi:[0,0,0]
	v_mfma_scale_f32_16x16x128_f8f6f4 v[126:129], v[2:9], v[216:223], v[126:129], v189, v190 op_sel_hi:[0,0,0]
	v_mfma_scale_f32_16x16x128_f8f6f4 v[118:121], v[10:17], v[216:223], v[118:121], v189, v190 op_sel_hi:[0,0,0]
	v_mfma_scale_f32_16x16x128_f8f6f4 v[110:113], v[2:9], v[224:231], v[110:113], v189, v190 op_sel_hi:[0,0,0]
	v_mfma_scale_f32_16x16x128_f8f6f4 v[102:105], v[10:17], v[224:231], v[102:105], v189, v190 op_sel_hi:[0,0,0]
	s_setprio 0
	s_setprio 1
	v_mfma_scale_f32_16x16x128_f8f6f4 v[154:157], v[18:25], v[192:199], v[154:157], v189, v190 op_sel_hi:[0,0,0]
	v_mfma_scale_f32_16x16x128_f8f6f4 v[146:149], v[26:33], v[192:199], v[146:149], v189, v190 op_sel_hi:[0,0,0]
	v_mfma_scale_f32_16x16x128_f8f6f4 v[138:141], v[18:25], v[200:207], v[138:141], v189, v190 op_sel_hi:[0,0,0]
	v_mfma_scale_f32_16x16x128_f8f6f4 v[130:133], v[26:33], v[200:207], v[130:133], v189, v190 op_sel_hi:[0,0,0]
	v_mfma_scale_f32_16x16x128_f8f6f4 v[122:125], v[18:25], v[216:223], v[122:125], v189, v190 op_sel_hi:[0,0,0]
	v_mfma_scale_f32_16x16x128_f8f6f4 v[114:117], v[26:33], v[216:223], v[114:117], v189, v190 op_sel_hi:[0,0,0]
	v_mfma_scale_f32_16x16x128_f8f6f4 v[106:109], v[18:25], v[224:231], v[106:109], v189, v190 op_sel_hi:[0,0,0]
	v_mfma_scale_f32_16x16x128_f8f6f4 v[98:101], v[26:33], v[224:231], v[98:101], v189, v190 op_sel_hi:[0,0,0]
	s_barrier
	s_setprio 0
	s_add_i32 s38, s71, s43
	v_lshl_add_u64 v[176:177], v[176:177], 0, s[12:13]
	s_mov_b32 m0, s38
	ds_read_b128 v[192:195], v188 offset:49152
	ds_read_b128 v[196:199], v188 offset:50176
	ds_read_b128 v[200:203], v188 offset:51200
	ds_read_b128 v[204:207], v188 offset:52224
	ds_read_b128 v[216:219], v188 offset:53248
	ds_read_b128 v[220:223], v188 offset:54272
	ds_read_b128 v[224:227], v188 offset:55296
	ds_read_b128 v[228:231], v188 offset:56320
	global_load_lds_dwordx4 v[176:177], off
	s_add_i32 m0, s38, 0x2000
	s_add_u32 s36, s36, 0x40080
	v_lshl_add_u64 v[176:177], v[178:179], 0, s[12:13]
	s_addc_u32 s37, s37, 0
	s_add_i32 s38, s72, s43
	global_load_lds_dwordx4 v[176:177], off
	v_lshl_add_u64 v[176:177], s[36:37], 0, v[166:167]
	s_mov_b32 m0, s38
	s_nop 0
	global_load_lds_dwordx4 v[176:177], off
	v_lshl_add_u64 v[176:177], s[36:37], 0, v[162:163]
	s_add_i32 m0, s38, 0x2000
	s_nop 0
	global_load_lds_dwordx4 v[176:177], off
	v_lshl_add_u64 v[176:177], v[180:181], 0, s[12:13]
	s_mov_b32 m0, s50
	s_nop 0
	global_load_lds_dwordx4 v[176:177], off
	v_lshl_add_u64 v[176:177], v[182:183], 0, s[12:13]
	s_mov_b32 m0, s51
	s_nop 0
	global_load_lds_dwordx4 v[176:177], off
	s_waitcnt vmcnt(8)
	s_waitcnt lgkmcnt(0)
	s_setprio 1
	s_barrier
	v_mfma_scale_f32_16x16x128_f8f6f4 v[94:97], v[2:9], v[192:199], v[94:97], v189, v190 op_sel_hi:[0,0,0]
	v_mfma_scale_f32_16x16x128_f8f6f4 v[86:89], v[10:17], v[192:199], v[86:89], v189, v190 op_sel_hi:[0,0,0]
	v_mfma_scale_f32_16x16x128_f8f6f4 v[78:81], v[2:9], v[200:207], v[78:81], v189, v190 op_sel_hi:[0,0,0]
	v_mfma_scale_f32_16x16x128_f8f6f4 v[70:73], v[10:17], v[200:207], v[70:73], v189, v190 op_sel_hi:[0,0,0]
	v_mfma_scale_f32_16x16x128_f8f6f4 v[62:65], v[2:9], v[216:223], v[62:65], v189, v190 op_sel_hi:[0,0,0]
	v_mfma_scale_f32_16x16x128_f8f6f4 v[54:57], v[10:17], v[216:223], v[54:57], v189, v190 op_sel_hi:[0,0,0]
	v_mfma_scale_f32_16x16x128_f8f6f4 v[46:49], v[2:9], v[224:231], v[46:49], v189, v190 op_sel_hi:[0,0,0]
	v_mfma_scale_f32_16x16x128_f8f6f4 v[38:41], v[10:17], v[224:231], v[38:41], v189, v190 op_sel_hi:[0,0,0]
	s_setprio 0
	s_setprio 1
	v_mfma_scale_f32_16x16x128_f8f6f4 v[90:93], v[18:25], v[192:199], v[90:93], v189, v190 op_sel_hi:[0,0,0]
	v_mfma_scale_f32_16x16x128_f8f6f4 v[82:85], v[26:33], v[192:199], v[82:85], v189, v190 op_sel_hi:[0,0,0]
	v_mfma_scale_f32_16x16x128_f8f6f4 v[74:77], v[18:25], v[200:207], v[74:77], v189, v190 op_sel_hi:[0,0,0]
	v_mfma_scale_f32_16x16x128_f8f6f4 v[66:69], v[26:33], v[200:207], v[66:69], v189, v190 op_sel_hi:[0,0,0]
	v_mfma_scale_f32_16x16x128_f8f6f4 v[58:61], v[18:25], v[216:223], v[58:61], v189, v190 op_sel_hi:[0,0,0]
	v_mfma_scale_f32_16x16x128_f8f6f4 v[50:53], v[26:33], v[216:223], v[50:53], v189, v190 op_sel_hi:[0,0,0]
	v_mfma_scale_f32_16x16x128_f8f6f4 v[42:45], v[18:25], v[224:231], v[42:45], v189, v190 op_sel_hi:[0,0,0]
	v_mfma_scale_f32_16x16x128_f8f6f4 v[34:37], v[26:33], v[224:231], v[34:37], v189, v190 op_sel_hi:[0,0,0]
	s_barrier
	s_setprio 0
	s_add_i32 s70, s70, 2
	s_add_u32 s34, s34, 0x100
	s_addc_u32 s35, s35, 0
	s_add_u32 s68, s68, 0x100
	s_addc_u32 s69, s69, 0
	s_cmp_gt_u32 s70, 13

.LBB0_2440:
	s_add_u32 s38, s38, 0xe0080
	s_addc_u32 s39, s39, 0
	v_lshl_add_u64 v[176:177], v[0:1], 0, s[26:27]
	s_mov_b32 s71, -2
	ds_read_b128 v[16:19], v191
	ds_read_b128 v[20:23], v191 offset:1024
	ds_read_b128 v[24:27], v191 offset:2048
	ds_read_b128 v[28:31], v191 offset:3072
	ds_read_b128 v[0:3], v192
	ds_read_b128 v[4:7], v192 offset:1024
	ds_read_b128 v[8:11], v192 offset:2048
	ds_read_b128 v[12:15], v192 offset:3072
	s_add_u32 s40, s38, 0xfff20080
	s_addc_u32 s41, s39, -1
	s_cmp_eq_u32 s71, 52
	s_cselect_b64 vcc, -1, 0
	s_cselect_b32 s41, s1, s41
	s_cselect_b32 s40, s0, s40
	v_cndmask_b32_e32 v179, v177, v175, vcc
	v_cndmask_b32_e32 v178, v176, v174, vcc
	v_lshl_add_u64 v[214:215], s[38:39], 0, v[168:169]
	s_add_i32 m0, s47, 0xc000
	ds_read_b128 v[180:183], v193
	ds_read_b128 v[184:187], v193 offset:1024
	ds_read_b128 v[198:201], v193 offset:2048
	ds_read_b128 v[202:205], v193 offset:3072
	ds_read_b128 v[206:209], v193 offset:4096
	ds_read_b128 v[210:213], v193 offset:5120
	ds_read_b128 v[216:219], v193 offset:6144
	ds_read_b128 v[220:223], v193 offset:7168
	global_load_lds_dwordx4 v[214:215], off
	v_lshl_add_u64 v[214:215], s[38:39], 0, v[170:171]
	s_add_i32 m0, s47, 0xe000
	s_nop 0
	global_load_lds_dwordx4 v[214:215], off
	s_waitcnt vmcnt(8)
	s_waitcnt lgkmcnt(0)
	s_setprio 1
	s_barrier
	v_mfma_scale_f32_16x16x128_f8f6f4 v[156:159], v[16:23], v[180:187], 0, v194, v195 op_sel_hi:[0,0,0]
	v_mfma_scale_f32_16x16x128_f8f6f4 v[152:155], v[24:31], v[180:187], 0, v194, v195 op_sel_hi:[0,0,0]
	v_mfma_scale_f32_16x16x128_f8f6f4 v[148:151], v[16:23], v[198:205], 0, v194, v195 op_sel_hi:[0,0,0]
	v_mfma_scale_f32_16x16x128_f8f6f4 v[140:143], v[24:31], v[198:205], 0, v194, v195 op_sel_hi:[0,0,0]
	v_mfma_scale_f32_16x16x128_f8f6f4 v[132:135], v[16:23], v[206:213], 0, v194, v195 op_sel_hi:[0,0,0]
	v_mfma_scale_f32_16x16x128_f8f6f4 v[124:127], v[24:31], v[206:213], 0, v194, v195 op_sel_hi:[0,0,0]
	v_mfma_scale_f32_16x16x128_f8f6f4 v[116:119], v[16:23], v[216:223], 0, v194, v195 op_sel_hi:[0,0,0]
	v_mfma_scale_f32_16x16x128_f8f6f4 v[108:111], v[24:31], v[216:223], 0, v194, v195 op_sel_hi:[0,0,0]
	s_setprio 0
	s_setprio 1
	v_mfma_scale_f32_16x16x128_f8f6f4 v[144:147], v[0:7], v[180:187], 0, v194, v195 op_sel_hi:[0,0,0]
	v_mfma_scale_f32_16x16x128_f8f6f4 v[136:139], v[8:15], v[180:187], 0, v194, v195 op_sel_hi:[0,0,0]
	v_mfma_scale_f32_16x16x128_f8f6f4 v[128:131], v[0:7], v[198:205], 0, v194, v195 op_sel_hi:[0,0,0]
	v_mfma_scale_f32_16x16x128_f8f6f4 v[120:123], v[8:15], v[198:205], 0, v194, v195 op_sel_hi:[0,0,0]
	v_mfma_scale_f32_16x16x128_f8f6f4 v[112:115], v[0:7], v[206:213], 0, v194, v195 op_sel_hi:[0,0,0]
	v_mfma_scale_f32_16x16x128_f8f6f4 v[104:107], v[8:15], v[206:213], 0, v194, v195 op_sel_hi:[0,0,0]
	v_mfma_scale_f32_16x16x128_f8f6f4 v[100:103], v[0:7], v[216:223], 0, v194, v195 op_sel_hi:[0,0,0]
	v_mfma_scale_f32_16x16x128_f8f6f4 v[96:99], v[8:15], v[216:223], 0, v194, v195 op_sel_hi:[0,0,0]
	s_barrier
	s_setprio 0
	s_add_i32 s72, s6, s44
	v_lshl_add_u64 v[180:181], v[178:179], 0, v[164:165]
	s_mov_b32 m0, s72
	ds_read_b128 v[198:201], v193 offset:16384
	ds_read_b128 v[202:205], v193 offset:17408
	ds_read_b128 v[206:209], v193 offset:18432
	ds_read_b128 v[210:213], v193 offset:19456
	ds_read_b128 v[216:219], v193 offset:20480
	ds_read_b128 v[220:223], v193 offset:21504
	ds_read_b128 v[224:227], v193 offset:22528
	ds_read_b128 v[228:231], v193 offset:23552
	global_load_lds_dwordx4 v[180:181], off
	v_lshl_add_u64 v[182:183], v[178:179], 0, v[160:161]
	s_add_i32 m0, s72, 0x2000
	v_lshl_add_u64 v[184:185], v[178:179], 0, s[10:11]
	s_add_i32 s72, s62, s44
	global_load_lds_dwordx4 v[182:183], off
	v_lshl_add_u64 v[186:187], v[184:185], 0, v[164:165]
	s_mov_b32 m0, s72
	v_lshl_add_u64 v[184:185], v[184:185], 0, v[160:161]
	global_load_lds_dwordx4 v[186:187], off
	s_add_i32 m0, s72, 0x2000
	v_lshl_add_u64 v[186:187], s[40:41], 0, v[162:163]
	global_load_lds_dwordx4 v[184:185], off
	v_lshl_add_u64 v[184:185], s[40:41], 0, v[166:167]
	s_mov_b32 m0, s47
	s_nop 0
	global_load_lds_dwordx4 v[184:185], off
	s_mov_b32 m0, s48
	s_nop 0
	global_load_lds_dwordx4 v[186:187], off
	s_waitcnt vmcnt(8)
	s_waitcnt lgkmcnt(0)
	s_setprio 1
	s_barrier
	v_mfma_scale_f32_16x16x128_f8f6f4 v[92:95], v[16:23], v[198:205], 0, v194, v195 op_sel_hi:[0,0,0]
	v_mfma_scale_f32_16x16x128_f8f6f4 v[88:91], v[24:31], v[198:205], 0, v194, v195 op_sel_hi:[0,0,0]
	v_mfma_scale_f32_16x16x128_f8f6f4 v[84:87], v[16:23], v[206:213], 0, v194, v195 op_sel_hi:[0,0,0]
	v_mfma_scale_f32_16x16x128_f8f6f4 v[76:79], v[24:31], v[206:213], 0, v194, v195 op_sel_hi:[0,0,0]
	v_mfma_scale_f32_16x16x128_f8f6f4 v[68:71], v[16:23], v[216:223], 0, v194, v195 op_sel_hi:[0,0,0]
	v_mfma_scale_f32_16x16x128_f8f6f4 v[60:63], v[24:31], v[216:223], 0, v194, v195 op_sel_hi:[0,0,0]
	v_mfma_scale_f32_16x16x128_f8f6f4 v[52:55], v[16:23], v[224:231], 0, v194, v195 op_sel_hi:[0,0,0]
	v_mfma_scale_f32_16x16x128_f8f6f4 v[44:47], v[24:31], v[224:231], 0, v194, v195 op_sel_hi:[0,0,0]
	s_setprio 0
	s_setprio 1
	v_mfma_scale_f32_16x16x128_f8f6f4 v[80:83], v[0:7], v[198:205], 0, v194, v195 op_sel_hi:[0,0,0]
	v_mfma_scale_f32_16x16x128_f8f6f4 v[72:75], v[8:15], v[198:205], 0, v194, v195 op_sel_hi:[0,0,0]
	v_mfma_scale_f32_16x16x128_f8f6f4 v[64:67], v[0:7], v[206:213], 0, v194, v195 op_sel_hi:[0,0,0]
	v_mfma_scale_f32_16x16x128_f8f6f4 v[56:59], v[8:15], v[206:213], 0, v194, v195 op_sel_hi:[0,0,0]
	v_mfma_scale_f32_16x16x128_f8f6f4 v[48:51], v[0:7], v[216:223], 0, v194, v195 op_sel_hi:[0,0,0]
	v_mfma_scale_f32_16x16x128_f8f6f4 v[40:43], v[8:15], v[216:223], 0, v194, v195 op_sel_hi:[0,0,0]
	v_mfma_scale_f32_16x16x128_f8f6f4 v[36:39], v[0:7], v[224:231], 0, v194, v195 op_sel_hi:[0,0,0]
	v_mfma_scale_f32_16x16x128_f8f6f4 v[32:35], v[8:15], v[224:231], 0, v194, v195 op_sel_hi:[0,0,0]
	s_barrier
	s_setprio 0
	s_add_i32 s72, 0, 0x18000
	s_add_i32 s73, 0, 0x1c000
	v_add_u32_e32 v12, s72, v189
	v_add_u32_e32 v28, s73, v189
	ds_read_b128 v[0:3], v12
	ds_read_b128 v[4:7], v12 offset:1024
	ds_read_b128 v[8:11], v12 offset:2048
	ds_read_b128 v[12:15], v12 offset:3072
	ds_read_b128 v[16:19], v28
	ds_read_b128 v[20:23], v28 offset:1024
	ds_read_b128 v[24:27], v28 offset:2048
	ds_read_b128 v[28:31], v28 offset:3072
	s_add_u32 s40, s40, 0xe0000
	s_addc_u32 s41, s41, 0
	s_mov_b32 m0, s49
	v_lshl_add_u64 v[214:215], s[40:41], 0, v[166:167]
	ds_read_b128 v[198:201], v193 offset:32768
	ds_read_b128 v[202:205], v193 offset:33792
	ds_read_b128 v[206:209], v193 offset:34816
	ds_read_b128 v[210:213], v193 offset:35840
	ds_read_b128 v[216:219], v193 offset:36864
	ds_read_b128 v[220:223], v193 offset:37888
	ds_read_b128 v[224:227], v193 offset:38912
	ds_read_b128 v[228:231], v193 offset:39936
	global_load_lds_dwordx4 v[214:215], off
	v_lshl_add_u64 v[214:215], s[40:41], 0, v[162:163]
	s_mov_b32 m0, s50
	s_nop 0
	global_load_lds_dwordx4 v[214:215], off
	s_waitcnt vmcnt(8)
	s_waitcnt lgkmcnt(0)
	s_setprio 1
	s_barrier
	v_mfma_scale_f32_16x16x128_f8f6f4 v[156:159], v[0:7], v[198:205], v[156:159], v194, v195 op_sel_hi:[0,0,0]
	v_mfma_scale_f32_16x16x128_f8f6f4 v[152:155], v[8:15], v[198:205], v[152:155], v194, v195 op_sel_hi:[0,0,0]
	v_mfma_scale_f32_16x16x128_f8f6f4 v[148:151], v[0:7], v[206:213], v[148:151], v194, v195 op_sel_hi:[0,0,0]
	v_mfma_scale_f32_16x16x128_f8f6f4 v[140:143], v[8:15], v[206:213], v[140:143], v194, v195 op_sel_hi:[0,0,0]
	v_mfma_scale_f32_16x16x128_f8f6f4 v[132:135], v[0:7], v[216:223], v[132:135], v194, v195 op_sel_hi:[0,0,0]
	v_mfma_scale_f32_16x16x128_f8f6f4 v[124:127], v[8:15], v[216:223], v[124:127], v194, v195 op_sel_hi:[0,0,0]
	v_mfma_scale_f32_16x16x128_f8f6f4 v[116:119], v[0:7], v[224:231], v[116:119], v194, v195 op_sel_hi:[0,0,0]
	v_mfma_scale_f32_16x16x128_f8f6f4 v[108:111], v[8:15], v[224:231], v[108:111], v194, v195 op_sel_hi:[0,0,0]
	s_setprio 0
	s_setprio 1
	v_mfma_scale_f32_16x16x128_f8f6f4 v[144:147], v[16:23], v[198:205], v[144:147], v194, v195 op_sel_hi:[0,0,0]
	v_mfma_scale_f32_16x16x128_f8f6f4 v[136:139], v[24:31], v[198:205], v[136:139], v194, v195 op_sel_hi:[0,0,0]
	v_mfma_scale_f32_16x16x128_f8f6f4 v[128:131], v[16:23], v[206:213], v[128:131], v194, v195 op_sel_hi:[0,0,0]
	v_mfma_scale_f32_16x16x128_f8f6f4 v[120:123], v[24:31], v[206:213], v[120:123], v194, v195 op_sel_hi:[0,0,0]
	v_mfma_scale_f32_16x16x128_f8f6f4 v[112:115], v[16:23], v[216:223], v[112:115], v194, v195 op_sel_hi:[0,0,0]
	v_mfma_scale_f32_16x16x128_f8f6f4 v[104:107], v[24:31], v[216:223], v[104:107], v194, v195 op_sel_hi:[0,0,0]
	v_mfma_scale_f32_16x16x128_f8f6f4 v[100:103], v[16:23], v[224:231], v[100:103], v194, v195 op_sel_hi:[0,0,0]
	v_mfma_scale_f32_16x16x128_f8f6f4 v[96:99], v[24:31], v[224:231], v[96:99], v194, v195 op_sel_hi:[0,0,0]
	s_barrier
	s_setprio 0
	s_add_i32 s40, s72, s44
	v_lshl_add_u64 v[180:181], v[180:181], 0, s[18:19]
	s_mov_b32 m0, s40
	ds_read_b128 v[198:201], v193 offset:49152
	ds_read_b128 v[202:205], v193 offset:50176
	ds_read_b128 v[206:209], v193 offset:51200
	ds_read_b128 v[210:213], v193 offset:52224
	ds_read_b128 v[216:219], v193 offset:53248
	ds_read_b128 v[220:223], v193 offset:54272
	ds_read_b128 v[224:227], v193 offset:55296
	ds_read_b128 v[228:231], v193 offset:56320
	global_load_lds_dwordx4 v[180:181], off
	v_lshl_add_u64 v[180:181], v[182:183], 0, s[18:19]
	s_add_i32 m0, s40, 0x2000
	v_lshl_add_u64 v[178:179], v[178:179], 0, s[22:23]
	s_add_i32 s40, s73, s44
	global_load_lds_dwordx4 v[180:181], off
	v_lshl_add_u64 v[180:181], v[178:179], 0, v[164:165]
	s_mov_b32 m0, s40
	v_lshl_add_u64 v[178:179], v[178:179], 0, v[160:161]
	global_load_lds_dwordx4 v[180:181], off
	s_add_i32 m0, s40, 0x2000
	s_nop 0
	global_load_lds_dwordx4 v[178:179], off
	v_lshl_add_u64 v[178:179], v[184:185], 0, s[18:19]
	s_mov_b32 m0, s59
	s_nop 0
	global_load_lds_dwordx4 v[178:179], off
	v_lshl_add_u64 v[178:179], v[186:187], 0, s[18:19]
	s_mov_b32 m0, s60
	s_nop 0
	global_load_lds_dwordx4 v[178:179], off
	s_waitcnt vmcnt(8)
	s_waitcnt lgkmcnt(0)
	s_setprio 1
	s_barrier
	v_mfma_scale_f32_16x16x128_f8f6f4 v[92:95], v[0:7], v[198:205], v[92:95], v194, v195 op_sel_hi:[0,0,0]
	v_mfma_scale_f32_16x16x128_f8f6f4 v[88:91], v[8:15], v[198:205], v[88:91], v194, v195 op_sel_hi:[0,0,0]
	v_mfma_scale_f32_16x16x128_f8f6f4 v[84:87], v[0:7], v[206:213], v[84:87], v194, v195 op_sel_hi:[0,0,0]
	v_mfma_scale_f32_16x16x128_f8f6f4 v[76:79], v[8:15], v[206:213], v[76:79], v194, v195 op_sel_hi:[0,0,0]
	v_mfma_scale_f32_16x16x128_f8f6f4 v[68:71], v[0:7], v[216:223], v[68:71], v194, v195 op_sel_hi:[0,0,0]
	v_mfma_scale_f32_16x16x128_f8f6f4 v[60:63], v[8:15], v[216:223], v[60:63], v194, v195 op_sel_hi:[0,0,0]
	v_mfma_scale_f32_16x16x128_f8f6f4 v[52:55], v[0:7], v[224:231], v[52:55], v194, v195 op_sel_hi:[0,0,0]
	v_mfma_scale_f32_16x16x128_f8f6f4 v[44:47], v[8:15], v[224:231], v[44:47], v194, v195 op_sel_hi:[0,0,0]
	s_setprio 0
	s_setprio 1
	v_mfma_scale_f32_16x16x128_f8f6f4 v[80:83], v[16:23], v[198:205], v[80:83], v194, v195 op_sel_hi:[0,0,0]
	v_mfma_scale_f32_16x16x128_f8f6f4 v[72:75], v[24:31], v[198:205], v[72:75], v194, v195 op_sel_hi:[0,0,0]
	v_mfma_scale_f32_16x16x128_f8f6f4 v[64:67], v[16:23], v[206:213], v[64:67], v194, v195 op_sel_hi:[0,0,0]
	v_mfma_scale_f32_16x16x128_f8f6f4 v[56:59], v[24:31], v[206:213], v[56:59], v194, v195 op_sel_hi:[0,0,0]
	v_mfma_scale_f32_16x16x128_f8f6f4 v[48:51], v[16:23], v[216:223], v[48:51], v194, v195 op_sel_hi:[0,0,0]
	v_mfma_scale_f32_16x16x128_f8f6f4 v[40:43], v[24:31], v[216:223], v[40:43], v194, v195 op_sel_hi:[0,0,0]
	v_mfma_scale_f32_16x16x128_f8f6f4 v[36:39], v[16:23], v[224:231], v[36:39], v194, v195 op_sel_hi:[0,0,0]
	v_mfma_scale_f32_16x16x128_f8f6f4 v[32:35], v[24:31], v[224:231], v[32:35], v194, v195 op_sel_hi:[0,0,0]
	s_barrier
	s_setprio 0
	s_add_i32 s71, s71, 2
	s_add_u32 s38, s38, 0x100
	s_addc_u32 s39, s39, 0
	s_cmp_gt_u32 s71, 53
	v_lshl_add_u64 v[176:177], v[176:177], 0, s[26:27]
